# GEMM loops: when a workgroup has no next unit, the next-unit prefetch LDS-DMAs of the last k-iteration are issued against an empty buffer descriptor (zero fill, no memory traffic)
# speedup vs baseline: 1.0011x; 1.0011x over previous
.LBB0_242:
	s_mov_b32 s98, s58
	ds_read_b128 v[132:135], v206
	ds_read_b128 v[136:139], v206 offset:1024
	ds_read_b128 v[140:143], v206 offset:2048
	ds_read_b128 v[144:147], v206 offset:3072
	ds_read_b128 v[148:151], v206 offset:16384
	ds_read_b128 v[152:155], v206 offset:17408
	ds_read_b128 v[156:159], v206 offset:18432
	ds_read_b128 v[160:163], v206 offset:19456
	s_add_i32 s3, s0, 0xfffc0080
	s_cmp_eq_u32 s2, 12
	s_cselect_b32 s9, s79, s3
	s_cselect_b32 s8, s85, s1
	s_add_i32 s3, s9, 0x80
	s_mov_b32 s56, s50
	s_mov_b32 m0, s54
	ds_read_b128 v[174:177], v207
	ds_read_b128 v[178:181], v207 offset:1024
	ds_read_b128 v[208:211], v207 offset:2048
	ds_read_b128 v[212:215], v207 offset:3072
	ds_read_b128 v[216:219], v207 offset:4096
	ds_read_b128 v[224:227], v207 offset:5120
	ds_read_b128 v[228:231], v207 offset:6144
	ds_read_b128 v[232:235], v207 offset:7168
	buffer_load_dwordx4 v166, s[56:59], s0 offen lds
	s_mov_b32 m0, s76
	s_nop 0
	buffer_load_dwordx4 v182, s[56:59], s0 offen lds
	s_waitcnt vmcnt(8)
	s_waitcnt lgkmcnt(0)
	s_barrier
	s_setprio 1
	s_waitcnt lgkmcnt(7)
	v_mfma_i32_16x16x64_i8 v[124:127], v[132:135], v[174:177], v[124:127]
	v_mfma_i32_16x16x64_i8 v[120:123], v[140:143], v[174:177], v[120:123]
	s_waitcnt lgkmcnt(5)
	v_mfma_i32_16x16x64_i8 v[116:119], v[132:135], v[208:211], v[116:119]
	v_mfma_i32_16x16x64_i8 v[112:115], v[140:143], v[208:211], v[112:115]
	s_waitcnt lgkmcnt(3)
	v_mfma_i32_16x16x64_i8 v[108:111], v[132:135], v[216:219], v[108:111]
	v_mfma_i32_16x16x64_i8 v[104:107], v[140:143], v[216:219], v[104:107]
	s_waitcnt lgkmcnt(1)
	v_mfma_i32_16x16x64_i8 v[100:103], v[132:135], v[228:231], v[100:103]
	v_mfma_i32_16x16x64_i8 v[96:99], v[140:143], v[228:231], v[96:99]
	v_mfma_i32_16x16x64_i8 v[124:127], v[136:139], v[178:181], v[124:127]
	v_mfma_i32_16x16x64_i8 v[120:123], v[144:147], v[178:181], v[120:123]
	v_mfma_i32_16x16x64_i8 v[116:119], v[136:139], v[212:215], v[116:119]
	v_mfma_i32_16x16x64_i8 v[112:115], v[144:147], v[212:215], v[112:115]
	v_mfma_i32_16x16x64_i8 v[108:111], v[136:139], v[224:227], v[108:111]
	v_mfma_i32_16x16x64_i8 v[104:107], v[144:147], v[224:227], v[104:107]
	s_waitcnt lgkmcnt(0)
	v_mfma_i32_16x16x64_i8 v[100:103], v[136:139], v[232:235], v[100:103]
	v_mfma_i32_16x16x64_i8 v[96:99], v[144:147], v[232:235], v[96:99]
	s_setprio 0
	s_setprio 1
	v_mfma_i32_16x16x64_i8 v[92:95], v[148:151], v[174:177], v[92:95]
	v_mfma_i32_16x16x64_i8 v[88:91], v[156:159], v[174:177], v[88:91]
	v_mfma_i32_16x16x64_i8 v[84:87], v[148:151], v[208:211], v[84:87]
	v_mfma_i32_16x16x64_i8 v[80:83], v[156:159], v[208:211], v[80:83]
	v_mfma_i32_16x16x64_i8 v[76:79], v[148:151], v[216:219], v[76:79]
	v_mfma_i32_16x16x64_i8 v[72:75], v[156:159], v[216:219], v[72:75]
	v_mfma_i32_16x16x64_i8 v[68:71], v[148:151], v[228:231], v[68:71]
	v_mfma_i32_16x16x64_i8 v[64:67], v[156:159], v[228:231], v[64:67]
	v_mfma_i32_16x16x64_i8 v[92:95], v[152:155], v[178:181], v[92:95]
	v_mfma_i32_16x16x64_i8 v[88:91], v[160:163], v[178:181], v[88:91]
	v_mfma_i32_16x16x64_i8 v[84:87], v[152:155], v[212:215], v[84:87]
	v_mfma_i32_16x16x64_i8 v[80:83], v[160:163], v[212:215], v[80:83]
	v_mfma_i32_16x16x64_i8 v[76:79], v[152:155], v[224:227], v[76:79]
	v_mfma_i32_16x16x64_i8 v[72:75], v[160:163], v[224:227], v[72:75]
	v_mfma_i32_16x16x64_i8 v[68:71], v[152:155], v[232:235], v[68:71]
	v_mfma_i32_16x16x64_i8 v[64:67], v[160:163], v[232:235], v[64:67]
	s_setprio 0
	s_barrier
	s_cmp_eq_u64 s[34:35], 0
	s_cselect_b32 s99, 12, -1
	s_cmp_eq_u32 s2, s99
	s_cselect_b32 s58, 0, s58
	s_mov_b32 m0, s26
	ds_read_b128 v[174:177], v207 offset:16384
	ds_read_b128 v[178:181], v207 offset:17408
	ds_read_b128 v[208:211], v207 offset:18432
	ds_read_b128 v[212:215], v207 offset:19456
	ds_read_b128 v[216:219], v207 offset:20480
	ds_read_b128 v[224:227], v207 offset:21504
	ds_read_b128 v[228:231], v207 offset:22528
	ds_read_b128 v[232:235], v207 offset:23552
	buffer_load_dwordx4 v167, s[56:59], s8 offen lds
	s_mov_b32 m0, s27
	s_add_i32 s12, s8, 0x40000
	buffer_load_dwordx4 v183, s[56:59], s8 offen lds
	s_mov_b32 m0, s28
	s_nop 0
	buffer_load_dwordx4 v167, s[56:59], s12 offen lds
	s_mov_b32 m0, s29
	s_nop 0
	buffer_load_dwordx4 v183, s[56:59], s12 offen lds
	s_mov_b32 m0, s25
	s_nop 0
	buffer_load_dwordx4 v166, s[56:59], s9 offen lds
	s_mov_b32 m0, s30
	s_nop 0
	buffer_load_dwordx4 v182, s[56:59], s9 offen lds
	s_waitcnt vmcnt(8)
	s_waitcnt lgkmcnt(0)
	s_barrier
	s_setprio 1
	s_waitcnt lgkmcnt(7)
	v_mfma_i32_16x16x64_i8 v[60:63], v[132:135], v[174:177], v[60:63]
	v_mfma_i32_16x16x64_i8 v[56:59], v[140:143], v[174:177], v[56:59]
	s_waitcnt lgkmcnt(5)
	v_mfma_i32_16x16x64_i8 v[52:55], v[132:135], v[208:211], v[52:55]
	v_mfma_i32_16x16x64_i8 v[48:51], v[140:143], v[208:211], v[48:51]
	s_waitcnt lgkmcnt(3)
	v_mfma_i32_16x16x64_i8 v[44:47], v[132:135], v[216:219], v[44:47]
	v_mfma_i32_16x16x64_i8 v[40:43], v[140:143], v[216:219], v[40:43]
	s_waitcnt lgkmcnt(1)
	v_mfma_i32_16x16x64_i8 v[36:39], v[132:135], v[228:231], v[36:39]
	v_mfma_i32_16x16x64_i8 v[32:35], v[140:143], v[228:231], v[32:35]
	v_mfma_i32_16x16x64_i8 v[60:63], v[136:139], v[178:181], v[60:63]
	v_mfma_i32_16x16x64_i8 v[56:59], v[144:147], v[178:181], v[56:59]
	v_mfma_i32_16x16x64_i8 v[52:55], v[136:139], v[212:215], v[52:55]
	v_mfma_i32_16x16x64_i8 v[48:51], v[144:147], v[212:215], v[48:51]
	v_mfma_i32_16x16x64_i8 v[44:47], v[136:139], v[224:227], v[44:47]
	v_mfma_i32_16x16x64_i8 v[40:43], v[144:147], v[224:227], v[40:43]
	s_waitcnt lgkmcnt(0)
	v_mfma_i32_16x16x64_i8 v[36:39], v[136:139], v[232:235], v[36:39]
	v_mfma_i32_16x16x64_i8 v[32:35], v[144:147], v[232:235], v[32:35]
	s_setprio 0
	s_setprio 1
	v_mfma_i32_16x16x64_i8 v[28:31], v[148:151], v[174:177], v[28:31]
	v_mfma_i32_16x16x64_i8 v[24:27], v[156:159], v[174:177], v[24:27]
	v_mfma_i32_16x16x64_i8 v[20:23], v[148:151], v[208:211], v[20:23]
	v_mfma_i32_16x16x64_i8 v[16:19], v[156:159], v[208:211], v[16:19]
	v_mfma_i32_16x16x64_i8 v[12:15], v[148:151], v[216:219], v[12:15]
	v_mfma_i32_16x16x64_i8 v[8:11], v[156:159], v[216:219], v[8:11]
	v_mfma_i32_16x16x64_i8 v[4:7], v[148:151], v[228:231], v[4:7]
	v_mfma_i32_16x16x64_i8 v[0:3], v[156:159], v[228:231], v[0:3]
	v_mfma_i32_16x16x64_i8 v[28:31], v[152:155], v[178:181], v[28:31]
	v_mfma_i32_16x16x64_i8 v[24:27], v[160:163], v[178:181], v[24:27]
	v_mfma_i32_16x16x64_i8 v[20:23], v[152:155], v[212:215], v[20:23]
	v_mfma_i32_16x16x64_i8 v[16:19], v[160:163], v[212:215], v[16:19]
	v_mfma_i32_16x16x64_i8 v[12:15], v[152:155], v[224:227], v[12:15]
	v_mfma_i32_16x16x64_i8 v[8:11], v[160:163], v[224:227], v[8:11]
	v_mfma_i32_16x16x64_i8 v[4:7], v[152:155], v[232:235], v[4:7]
	v_mfma_i32_16x16x64_i8 v[0:3], v[160:163], v[232:235], v[0:3]
	s_setprio 0
	s_barrier
	ds_read_b128 v[132:135], v206 offset:32768
	ds_read_b128 v[136:139], v206 offset:33792
	ds_read_b128 v[140:143], v206 offset:34816
	ds_read_b128 v[144:147], v206 offset:35840
	ds_read_b128 v[148:151], v206 offset:49152
	ds_read_b128 v[152:155], v206 offset:50176
	ds_read_b128 v[156:159], v206 offset:51200
	ds_read_b128 v[160:163], v206 offset:52224
	s_add_i32 s9, s9, 0x40000
	s_mov_b32 m0, s31
	ds_read_b128 v[174:177], v207 offset:32768
	ds_read_b128 v[178:181], v207 offset:33792
	ds_read_b128 v[208:211], v207 offset:34816
	ds_read_b128 v[212:215], v207 offset:35840
	ds_read_b128 v[216:219], v207 offset:36864
	ds_read_b128 v[224:227], v207 offset:37888
	ds_read_b128 v[228:231], v207 offset:38912
	ds_read_b128 v[232:235], v207 offset:39936
	buffer_load_dwordx4 v166, s[56:59], s9 offen lds
	s_mov_b32 m0, s33
	s_nop 0
	buffer_load_dwordx4 v182, s[56:59], s9 offen lds
	s_waitcnt vmcnt(8)
	s_waitcnt lgkmcnt(0)
	s_barrier
	s_setprio 1
	s_waitcnt lgkmcnt(7)
	v_mfma_i32_16x16x64_i8 v[124:127], v[132:135], v[174:177], v[124:127]
	v_mfma_i32_16x16x64_i8 v[120:123], v[140:143], v[174:177], v[120:123]
	s_waitcnt lgkmcnt(5)
	v_mfma_i32_16x16x64_i8 v[116:119], v[132:135], v[208:211], v[116:119]
	v_mfma_i32_16x16x64_i8 v[112:115], v[140:143], v[208:211], v[112:115]
	s_waitcnt lgkmcnt(3)
	v_mfma_i32_16x16x64_i8 v[108:111], v[132:135], v[216:219], v[108:111]
	v_mfma_i32_16x16x64_i8 v[104:107], v[140:143], v[216:219], v[104:107]
	s_waitcnt lgkmcnt(1)
	v_mfma_i32_16x16x64_i8 v[100:103], v[132:135], v[228:231], v[100:103]
	v_mfma_i32_16x16x64_i8 v[96:99], v[140:143], v[228:231], v[96:99]
	v_mfma_i32_16x16x64_i8 v[124:127], v[136:139], v[178:181], v[124:127]
	v_mfma_i32_16x16x64_i8 v[120:123], v[144:147], v[178:181], v[120:123]
	v_mfma_i32_16x16x64_i8 v[116:119], v[136:139], v[212:215], v[116:119]
	v_mfma_i32_16x16x64_i8 v[112:115], v[144:147], v[212:215], v[112:115]
	v_mfma_i32_16x16x64_i8 v[108:111], v[136:139], v[224:227], v[108:111]
	v_mfma_i32_16x16x64_i8 v[104:107], v[144:147], v[224:227], v[104:107]
	s_waitcnt lgkmcnt(0)
	v_mfma_i32_16x16x64_i8 v[100:103], v[136:139], v[232:235], v[100:103]
	v_mfma_i32_16x16x64_i8 v[96:99], v[144:147], v[232:235], v[96:99]
	s_setprio 0
	s_setprio 1
	v_mfma_i32_16x16x64_i8 v[92:95], v[148:151], v[174:177], v[92:95]
	v_mfma_i32_16x16x64_i8 v[88:91], v[156:159], v[174:177], v[88:91]
	v_mfma_i32_16x16x64_i8 v[84:87], v[148:151], v[208:211], v[84:87]
	v_mfma_i32_16x16x64_i8 v[80:83], v[156:159], v[208:211], v[80:83]
	v_mfma_i32_16x16x64_i8 v[76:79], v[148:151], v[216:219], v[76:79]
	v_mfma_i32_16x16x64_i8 v[72:75], v[156:159], v[216:219], v[72:75]
	v_mfma_i32_16x16x64_i8 v[68:71], v[148:151], v[228:231], v[68:71]
	v_mfma_i32_16x16x64_i8 v[64:67], v[156:159], v[228:231], v[64:67]
	v_mfma_i32_16x16x64_i8 v[92:95], v[152:155], v[178:181], v[92:95]
	v_mfma_i32_16x16x64_i8 v[88:91], v[160:163], v[178:181], v[88:91]
	v_mfma_i32_16x16x64_i8 v[84:87], v[152:155], v[212:215], v[84:87]
	v_mfma_i32_16x16x64_i8 v[80:83], v[160:163], v[212:215], v[80:83]
	v_mfma_i32_16x16x64_i8 v[76:79], v[152:155], v[224:227], v[76:79]
	v_mfma_i32_16x16x64_i8 v[72:75], v[160:163], v[224:227], v[72:75]
	v_mfma_i32_16x16x64_i8 v[68:71], v[152:155], v[232:235], v[68:71]
	v_mfma_i32_16x16x64_i8 v[64:67], v[160:163], v[232:235], v[64:67]
	s_setprio 0
	s_barrier
	s_mov_b32 m0, s61
	s_add_i32 s9, s8, 0x80
	ds_read_b128 v[174:177], v207 offset:49152
	ds_read_b128 v[178:181], v207 offset:50176
	ds_read_b128 v[208:211], v207 offset:51200
	ds_read_b128 v[212:215], v207 offset:52224
	ds_read_b128 v[216:219], v207 offset:53248
	ds_read_b128 v[224:227], v207 offset:54272
	ds_read_b128 v[228:231], v207 offset:55296
	ds_read_b128 v[232:235], v207 offset:56320
	buffer_load_dwordx4 v167, s[56:59], s9 offen lds
	s_mov_b32 m0, s62
	s_add_i32 s8, s8, 0x40080
	buffer_load_dwordx4 v183, s[56:59], s9 offen lds
	s_mov_b32 m0, s52
	s_nop 0
	buffer_load_dwordx4 v167, s[56:59], s8 offen lds
	s_mov_b32 m0, s53
	s_nop 0
	buffer_load_dwordx4 v183, s[56:59], s8 offen lds
	s_mov_b32 m0, s63
	s_nop 0
	buffer_load_dwordx4 v166, s[56:59], s3 offen lds
	s_mov_b32 m0, s64
	s_nop 0
	buffer_load_dwordx4 v182, s[56:59], s3 offen lds
	s_waitcnt vmcnt(8)
	s_waitcnt lgkmcnt(0)
	s_barrier
	s_setprio 1
	s_waitcnt lgkmcnt(7)
	v_mfma_i32_16x16x64_i8 v[60:63], v[132:135], v[174:177], v[60:63]
	v_mfma_i32_16x16x64_i8 v[56:59], v[140:143], v[174:177], v[56:59]
	s_waitcnt lgkmcnt(5)
	v_mfma_i32_16x16x64_i8 v[52:55], v[132:135], v[208:211], v[52:55]
	v_mfma_i32_16x16x64_i8 v[48:51], v[140:143], v[208:211], v[48:51]
	s_waitcnt lgkmcnt(3)
	v_mfma_i32_16x16x64_i8 v[44:47], v[132:135], v[216:219], v[44:47]
	v_mfma_i32_16x16x64_i8 v[40:43], v[140:143], v[216:219], v[40:43]
	s_waitcnt lgkmcnt(1)
	v_mfma_i32_16x16x64_i8 v[36:39], v[132:135], v[228:231], v[36:39]
	v_mfma_i32_16x16x64_i8 v[32:35], v[140:143], v[228:231], v[32:35]
	v_mfma_i32_16x16x64_i8 v[60:63], v[136:139], v[178:181], v[60:63]
	v_mfma_i32_16x16x64_i8 v[56:59], v[144:147], v[178:181], v[56:59]
	v_mfma_i32_16x16x64_i8 v[52:55], v[136:139], v[212:215], v[52:55]
	v_mfma_i32_16x16x64_i8 v[48:51], v[144:147], v[212:215], v[48:51]
	v_mfma_i32_16x16x64_i8 v[44:47], v[136:139], v[224:227], v[44:47]
	v_mfma_i32_16x16x64_i8 v[40:43], v[144:147], v[224:227], v[40:43]
	s_waitcnt lgkmcnt(0)
	v_mfma_i32_16x16x64_i8 v[36:39], v[136:139], v[232:235], v[36:39]
	v_mfma_i32_16x16x64_i8 v[32:35], v[144:147], v[232:235], v[32:35]
	s_setprio 0
	s_setprio 1
	v_mfma_i32_16x16x64_i8 v[28:31], v[148:151], v[174:177], v[28:31]
	v_mfma_i32_16x16x64_i8 v[24:27], v[156:159], v[174:177], v[24:27]
	v_mfma_i32_16x16x64_i8 v[20:23], v[148:151], v[208:211], v[20:23]
	v_mfma_i32_16x16x64_i8 v[16:19], v[156:159], v[208:211], v[16:19]
	v_mfma_i32_16x16x64_i8 v[12:15], v[148:151], v[216:219], v[12:15]
	v_mfma_i32_16x16x64_i8 v[8:11], v[156:159], v[216:219], v[8:11]
	v_mfma_i32_16x16x64_i8 v[4:7], v[148:151], v[228:231], v[4:7]
	v_mfma_i32_16x16x64_i8 v[0:3], v[156:159], v[228:231], v[0:3]
	v_mfma_i32_16x16x64_i8 v[28:31], v[152:155], v[178:181], v[28:31]
	v_mfma_i32_16x16x64_i8 v[24:27], v[160:163], v[178:181], v[24:27]
	v_mfma_i32_16x16x64_i8 v[20:23], v[152:155], v[212:215], v[20:23]
	v_mfma_i32_16x16x64_i8 v[16:19], v[160:163], v[212:215], v[16:19]
	v_mfma_i32_16x16x64_i8 v[12:15], v[152:155], v[224:227], v[12:15]
	v_mfma_i32_16x16x64_i8 v[8:11], v[160:163], v[224:227], v[8:11]
	v_mfma_i32_16x16x64_i8 v[4:7], v[152:155], v[232:235], v[4:7]
	v_mfma_i32_16x16x64_i8 v[0:3], v[160:163], v[232:235], v[0:3]
	s_setprio 0
	s_barrier
	s_add_i32 s2, s2, 2
	s_addk_i32 s0, 0x100
	s_addk_i32 s1, 0x100
	s_cmp_gt_u32 s2, 13
	s_cbranch_scc0 .LBB0_242
	s_mov_b32 s58, s98
	s_and_b64 vcc, exec, s[18:19]
	s_cbranch_vccz .LBB0_245
	s_barrier

.LBB0_710:
	s_mov_b32 s98, s58
	ds_read_b128 v[130:133], v143
	ds_read_b128 v[146:149], v143 offset:1024
	ds_read_b128 v[150:153], v143 offset:2048
	ds_read_b128 v[154:157], v143 offset:3072
	ds_read_b128 v[164:167], v143 offset:16384
	ds_read_b128 v[174:177], v143 offset:17408
	ds_read_b128 v[178:181], v143 offset:18432
	ds_read_b128 v[182:185], v143 offset:19456
	s_add_i32 s13, s8, 0xfff00080
	s_cmp_eq_u32 s12, 60
	s_cselect_b32 s15, s53, s13
	s_cselect_b32 s14, s54, s9
	s_add_i32 s13, s15, 0x80
	s_mov_b32 s56, s78
	s_mov_b32 m0, s46
	ds_read_b128 v[198:201], v144
	ds_read_b128 v[202:205], v144 offset:1024
	ds_read_b128 v[206:209], v144 offset:2048
	ds_read_b128 v[210:213], v144 offset:3072
	ds_read_b128 v[214:217], v144 offset:4096
	ds_read_b128 v[224:227], v144 offset:5120
	ds_read_b128 v[228:231], v144 offset:6144
	ds_read_b128 v[232:235], v144 offset:7168
	buffer_load_dwordx4 v129, s[56:59], s8 offen lds
	s_mov_b32 m0, s48
	s_nop 0
	buffer_load_dwordx4 v137, s[56:59], s8 offen lds
	s_waitcnt vmcnt(8)
	s_waitcnt lgkmcnt(0)
	s_barrier
	s_setprio 1
	s_waitcnt lgkmcnt(7)
	v_mfma_f32_16x16x32_bf16 v[124:127], v[130:133], v[198:201], v[124:127]
	v_mfma_f32_16x16x32_bf16 v[120:123], v[150:153], v[198:201], v[120:123]
	s_waitcnt lgkmcnt(5)
	v_mfma_f32_16x16x32_bf16 v[108:111], v[130:133], v[206:209], v[108:111]
	v_mfma_f32_16x16x32_bf16 v[104:107], v[150:153], v[206:209], v[104:107]
	s_waitcnt lgkmcnt(3)
	v_mfma_f32_16x16x32_bf16 v[92:95], v[130:133], v[214:217], v[92:95]
	v_mfma_f32_16x16x32_bf16 v[88:91], v[150:153], v[214:217], v[88:91]
	s_waitcnt lgkmcnt(1)
	v_mfma_f32_16x16x32_bf16 v[76:79], v[130:133], v[228:231], v[76:79]
	v_mfma_f32_16x16x32_bf16 v[72:75], v[150:153], v[228:231], v[72:75]
	v_mfma_f32_16x16x32_bf16 v[124:127], v[146:149], v[202:205], v[124:127]
	v_mfma_f32_16x16x32_bf16 v[120:123], v[154:157], v[202:205], v[120:123]
	v_mfma_f32_16x16x32_bf16 v[108:111], v[146:149], v[210:213], v[108:111]
	v_mfma_f32_16x16x32_bf16 v[104:107], v[154:157], v[210:213], v[104:107]
	v_mfma_f32_16x16x32_bf16 v[92:95], v[146:149], v[224:227], v[92:95]
	v_mfma_f32_16x16x32_bf16 v[88:91], v[154:157], v[224:227], v[88:91]
	s_waitcnt lgkmcnt(0)
	v_mfma_f32_16x16x32_bf16 v[76:79], v[146:149], v[232:235], v[76:79]
	v_mfma_f32_16x16x32_bf16 v[72:75], v[154:157], v[232:235], v[72:75]
	s_setprio 0
	s_setprio 1
	v_mfma_f32_16x16x32_bf16 v[116:119], v[164:167], v[198:201], v[116:119]
	v_mfma_f32_16x16x32_bf16 v[112:115], v[178:181], v[198:201], v[112:115]
	v_mfma_f32_16x16x32_bf16 v[100:103], v[164:167], v[206:209], v[100:103]
	v_mfma_f32_16x16x32_bf16 v[96:99], v[178:181], v[206:209], v[96:99]
	v_mfma_f32_16x16x32_bf16 v[84:87], v[164:167], v[214:217], v[84:87]
	v_mfma_f32_16x16x32_bf16 v[80:83], v[178:181], v[214:217], v[80:83]
	v_mfma_f32_16x16x32_bf16 v[68:71], v[164:167], v[228:231], v[68:71]
	v_mfma_f32_16x16x32_bf16 v[64:67], v[178:181], v[228:231], v[64:67]
	v_mfma_f32_16x16x32_bf16 v[116:119], v[174:177], v[202:205], v[116:119]
	v_mfma_f32_16x16x32_bf16 v[112:115], v[182:185], v[202:205], v[112:115]
	v_mfma_f32_16x16x32_bf16 v[100:103], v[174:177], v[210:213], v[100:103]
	v_mfma_f32_16x16x32_bf16 v[96:99], v[182:185], v[210:213], v[96:99]
	v_mfma_f32_16x16x32_bf16 v[84:87], v[174:177], v[224:227], v[84:87]
	v_mfma_f32_16x16x32_bf16 v[80:83], v[182:185], v[224:227], v[80:83]
	v_mfma_f32_16x16x32_bf16 v[68:71], v[174:177], v[232:235], v[68:71]
	v_mfma_f32_16x16x32_bf16 v[64:67], v[182:185], v[232:235], v[64:67]
	s_setprio 0
	s_barrier
	s_cmp_eq_u64 s[40:41], 0
	s_cselect_b32 s99, 60, -1
	s_cmp_eq_u32 s12, s99
	s_cselect_b32 s58, 0, s58
	s_mov_b32 m0, s21
	ds_read_b128 v[198:201], v144 offset:16384
	ds_read_b128 v[202:205], v144 offset:17408
	ds_read_b128 v[206:209], v144 offset:18432
	ds_read_b128 v[210:213], v144 offset:19456
	ds_read_b128 v[214:217], v144 offset:20480
	ds_read_b128 v[224:227], v144 offset:21504
	ds_read_b128 v[228:231], v144 offset:22528
	ds_read_b128 v[232:235], v144 offset:23552
	buffer_load_dwordx4 v136, s[56:59], s14 offen lds
	s_mov_b32 m0, s22
	s_add_i32 s33, s14, 0x100000
	buffer_load_dwordx4 v138, s[56:59], s14 offen lds
	s_mov_b32 m0, s23
	s_nop 0
	buffer_load_dwordx4 v136, s[56:59], s33 offen lds
	s_mov_b32 m0, s24
	s_nop 0
	buffer_load_dwordx4 v138, s[56:59], s33 offen lds
	s_mov_b32 m0, s20
	s_nop 0
	buffer_load_dwordx4 v129, s[56:59], s15 offen lds
	s_mov_b32 m0, s25
	s_nop 0
	buffer_load_dwordx4 v137, s[56:59], s15 offen lds
	s_waitcnt vmcnt(8)
	s_waitcnt lgkmcnt(0)
	s_barrier
	s_setprio 1
	s_waitcnt lgkmcnt(7)
	v_mfma_f32_16x16x32_bf16 v[60:63], v[130:133], v[198:201], v[60:63]
	v_mfma_f32_16x16x32_bf16 v[56:59], v[150:153], v[198:201], v[56:59]
	s_waitcnt lgkmcnt(5)
	v_mfma_f32_16x16x32_bf16 v[44:47], v[130:133], v[206:209], v[44:47]
	v_mfma_f32_16x16x32_bf16 v[40:43], v[150:153], v[206:209], v[40:43]
	s_waitcnt lgkmcnt(3)
	v_mfma_f32_16x16x32_bf16 v[28:31], v[130:133], v[214:217], v[28:31]
	v_mfma_f32_16x16x32_bf16 v[24:27], v[150:153], v[214:217], v[24:27]
	s_waitcnt lgkmcnt(1)
	v_mfma_f32_16x16x32_bf16 v[12:15], v[130:133], v[228:231], v[12:15]
	v_mfma_f32_16x16x32_bf16 v[8:11], v[150:153], v[228:231], v[8:11]
	v_mfma_f32_16x16x32_bf16 v[60:63], v[146:149], v[202:205], v[60:63]
	v_mfma_f32_16x16x32_bf16 v[56:59], v[154:157], v[202:205], v[56:59]
	v_mfma_f32_16x16x32_bf16 v[44:47], v[146:149], v[210:213], v[44:47]
	v_mfma_f32_16x16x32_bf16 v[40:43], v[154:157], v[210:213], v[40:43]
	v_mfma_f32_16x16x32_bf16 v[28:31], v[146:149], v[224:227], v[28:31]
	v_mfma_f32_16x16x32_bf16 v[24:27], v[154:157], v[224:227], v[24:27]
	s_waitcnt lgkmcnt(0)
	v_mfma_f32_16x16x32_bf16 v[12:15], v[146:149], v[232:235], v[12:15]
	v_mfma_f32_16x16x32_bf16 v[8:11], v[154:157], v[232:235], v[8:11]
	s_setprio 0
	s_setprio 1
	v_mfma_f32_16x16x32_bf16 v[52:55], v[164:167], v[198:201], v[52:55]
	v_mfma_f32_16x16x32_bf16 v[48:51], v[178:181], v[198:201], v[48:51]
	v_mfma_f32_16x16x32_bf16 v[36:39], v[164:167], v[206:209], v[36:39]
	v_mfma_f32_16x16x32_bf16 v[32:35], v[178:181], v[206:209], v[32:35]
	v_mfma_f32_16x16x32_bf16 v[20:23], v[164:167], v[214:217], v[20:23]
	v_mfma_f32_16x16x32_bf16 v[16:19], v[178:181], v[214:217], v[16:19]
	v_mfma_f32_16x16x32_bf16 v[4:7], v[164:167], v[228:231], v[4:7]
	v_mfma_f32_16x16x32_bf16 v[0:3], v[178:181], v[228:231], v[0:3]
	v_mfma_f32_16x16x32_bf16 v[52:55], v[174:177], v[202:205], v[52:55]
	v_mfma_f32_16x16x32_bf16 v[48:51], v[182:185], v[202:205], v[48:51]
	v_mfma_f32_16x16x32_bf16 v[36:39], v[174:177], v[210:213], v[36:39]
	v_mfma_f32_16x16x32_bf16 v[32:35], v[182:185], v[210:213], v[32:35]
	v_mfma_f32_16x16x32_bf16 v[20:23], v[174:177], v[224:227], v[20:23]
	v_mfma_f32_16x16x32_bf16 v[16:19], v[182:185], v[224:227], v[16:19]
	v_mfma_f32_16x16x32_bf16 v[4:7], v[174:177], v[232:235], v[4:7]
	v_mfma_f32_16x16x32_bf16 v[0:3], v[182:185], v[232:235], v[0:3]
	s_setprio 0
	s_barrier
	ds_read_b128 v[130:133], v143 offset:32768
	ds_read_b128 v[146:149], v143 offset:33792
	ds_read_b128 v[150:153], v143 offset:34816
	ds_read_b128 v[154:157], v143 offset:35840
	ds_read_b128 v[164:167], v143 offset:49152
	ds_read_b128 v[174:177], v143 offset:50176
	ds_read_b128 v[178:181], v143 offset:51200
	ds_read_b128 v[182:185], v143 offset:52224
	s_add_i32 s15, s15, 0x100000
	s_mov_b32 m0, s26
	ds_read_b128 v[198:201], v144 offset:32768
	ds_read_b128 v[202:205], v144 offset:33792
	ds_read_b128 v[206:209], v144 offset:34816
	ds_read_b128 v[210:213], v144 offset:35840
	ds_read_b128 v[214:217], v144 offset:36864
	ds_read_b128 v[224:227], v144 offset:37888
	ds_read_b128 v[228:231], v144 offset:38912
	ds_read_b128 v[232:235], v144 offset:39936
	buffer_load_dwordx4 v129, s[56:59], s15 offen lds
	s_mov_b32 m0, s27
	s_nop 0
	buffer_load_dwordx4 v137, s[56:59], s15 offen lds
	s_waitcnt vmcnt(8)
	s_waitcnt lgkmcnt(0)
	s_barrier
	s_setprio 1
	s_waitcnt lgkmcnt(7)
	v_mfma_f32_16x16x32_bf16 v[124:127], v[130:133], v[198:201], v[124:127]
	v_mfma_f32_16x16x32_bf16 v[120:123], v[150:153], v[198:201], v[120:123]
	s_waitcnt lgkmcnt(5)
	v_mfma_f32_16x16x32_bf16 v[108:111], v[130:133], v[206:209], v[108:111]
	v_mfma_f32_16x16x32_bf16 v[104:107], v[150:153], v[206:209], v[104:107]
	s_waitcnt lgkmcnt(3)
	v_mfma_f32_16x16x32_bf16 v[92:95], v[130:133], v[214:217], v[92:95]
	v_mfma_f32_16x16x32_bf16 v[88:91], v[150:153], v[214:217], v[88:91]
	s_waitcnt lgkmcnt(1)
	v_mfma_f32_16x16x32_bf16 v[76:79], v[130:133], v[228:231], v[76:79]
	v_mfma_f32_16x16x32_bf16 v[72:75], v[150:153], v[228:231], v[72:75]
	v_mfma_f32_16x16x32_bf16 v[124:127], v[146:149], v[202:205], v[124:127]
	v_mfma_f32_16x16x32_bf16 v[120:123], v[154:157], v[202:205], v[120:123]
	v_mfma_f32_16x16x32_bf16 v[108:111], v[146:149], v[210:213], v[108:111]
	v_mfma_f32_16x16x32_bf16 v[104:107], v[154:157], v[210:213], v[104:107]
	v_mfma_f32_16x16x32_bf16 v[92:95], v[146:149], v[224:227], v[92:95]
	v_mfma_f32_16x16x32_bf16 v[88:91], v[154:157], v[224:227], v[88:91]
	s_waitcnt lgkmcnt(0)
	v_mfma_f32_16x16x32_bf16 v[76:79], v[146:149], v[232:235], v[76:79]
	v_mfma_f32_16x16x32_bf16 v[72:75], v[154:157], v[232:235], v[72:75]
	s_setprio 0
	s_setprio 1
	v_mfma_f32_16x16x32_bf16 v[116:119], v[164:167], v[198:201], v[116:119]
	v_mfma_f32_16x16x32_bf16 v[112:115], v[178:181], v[198:201], v[112:115]
	v_mfma_f32_16x16x32_bf16 v[100:103], v[164:167], v[206:209], v[100:103]
	v_mfma_f32_16x16x32_bf16 v[96:99], v[178:181], v[206:209], v[96:99]
	v_mfma_f32_16x16x32_bf16 v[84:87], v[164:167], v[214:217], v[84:87]
	v_mfma_f32_16x16x32_bf16 v[80:83], v[178:181], v[214:217], v[80:83]
	v_mfma_f32_16x16x32_bf16 v[68:71], v[164:167], v[228:231], v[68:71]
	v_mfma_f32_16x16x32_bf16 v[64:67], v[178:181], v[228:231], v[64:67]
	v_mfma_f32_16x16x32_bf16 v[116:119], v[174:177], v[202:205], v[116:119]
	v_mfma_f32_16x16x32_bf16 v[112:115], v[182:185], v[202:205], v[112:115]
	v_mfma_f32_16x16x32_bf16 v[100:103], v[174:177], v[210:213], v[100:103]
	v_mfma_f32_16x16x32_bf16 v[96:99], v[182:185], v[210:213], v[96:99]
	v_mfma_f32_16x16x32_bf16 v[84:87], v[174:177], v[224:227], v[84:87]
	v_mfma_f32_16x16x32_bf16 v[80:83], v[182:185], v[224:227], v[80:83]
	v_mfma_f32_16x16x32_bf16 v[68:71], v[174:177], v[232:235], v[68:71]
	v_mfma_f32_16x16x32_bf16 v[64:67], v[182:185], v[232:235], v[64:67]
	s_setprio 0
	s_barrier
	s_mov_b32 m0, s29
	s_add_i32 s15, s14, 0x80
	ds_read_b128 v[198:201], v144 offset:49152
	ds_read_b128 v[202:205], v144 offset:50176
	ds_read_b128 v[206:209], v144 offset:51200
	ds_read_b128 v[210:213], v144 offset:52224
	ds_read_b128 v[214:217], v144 offset:53248
	ds_read_b128 v[224:227], v144 offset:54272
	ds_read_b128 v[228:231], v144 offset:55296
	ds_read_b128 v[232:235], v144 offset:56320
	buffer_load_dwordx4 v136, s[56:59], s15 offen lds
	s_mov_b32 m0, s30
	s_add_i32 s14, s14, 0x100080
	buffer_load_dwordx4 v138, s[56:59], s15 offen lds
	s_mov_b32 m0, s37
	s_nop 0
	buffer_load_dwordx4 v136, s[56:59], s14 offen lds
	s_mov_b32 m0, s45
	s_nop 0
	buffer_load_dwordx4 v138, s[56:59], s14 offen lds
	s_mov_b32 m0, s31
	s_nop 0
	buffer_load_dwordx4 v129, s[56:59], s13 offen lds
	s_mov_b32 m0, s36
	s_nop 0
	buffer_load_dwordx4 v137, s[56:59], s13 offen lds
	s_waitcnt vmcnt(8)
	s_waitcnt lgkmcnt(0)
	s_barrier
	s_setprio 1
	s_waitcnt lgkmcnt(7)
	v_mfma_f32_16x16x32_bf16 v[60:63], v[130:133], v[198:201], v[60:63]
	v_mfma_f32_16x16x32_bf16 v[56:59], v[150:153], v[198:201], v[56:59]
	s_waitcnt lgkmcnt(5)
	v_mfma_f32_16x16x32_bf16 v[44:47], v[130:133], v[206:209], v[44:47]
	v_mfma_f32_16x16x32_bf16 v[40:43], v[150:153], v[206:209], v[40:43]
	s_waitcnt lgkmcnt(3)
	v_mfma_f32_16x16x32_bf16 v[28:31], v[130:133], v[214:217], v[28:31]
	v_mfma_f32_16x16x32_bf16 v[24:27], v[150:153], v[214:217], v[24:27]
	s_waitcnt lgkmcnt(1)
	v_mfma_f32_16x16x32_bf16 v[12:15], v[130:133], v[228:231], v[12:15]
	v_mfma_f32_16x16x32_bf16 v[8:11], v[150:153], v[228:231], v[8:11]
	v_mfma_f32_16x16x32_bf16 v[60:63], v[146:149], v[202:205], v[60:63]
	v_mfma_f32_16x16x32_bf16 v[56:59], v[154:157], v[202:205], v[56:59]
	v_mfma_f32_16x16x32_bf16 v[44:47], v[146:149], v[210:213], v[44:47]
	v_mfma_f32_16x16x32_bf16 v[40:43], v[154:157], v[210:213], v[40:43]
	v_mfma_f32_16x16x32_bf16 v[28:31], v[146:149], v[224:227], v[28:31]
	v_mfma_f32_16x16x32_bf16 v[24:27], v[154:157], v[224:227], v[24:27]
	s_waitcnt lgkmcnt(0)
	v_mfma_f32_16x16x32_bf16 v[12:15], v[146:149], v[232:235], v[12:15]
	v_mfma_f32_16x16x32_bf16 v[8:11], v[154:157], v[232:235], v[8:11]
	s_setprio 0
	s_setprio 1
	v_mfma_f32_16x16x32_bf16 v[52:55], v[164:167], v[198:201], v[52:55]
	v_mfma_f32_16x16x32_bf16 v[48:51], v[178:181], v[198:201], v[48:51]
	v_mfma_f32_16x16x32_bf16 v[36:39], v[164:167], v[206:209], v[36:39]
	v_mfma_f32_16x16x32_bf16 v[32:35], v[178:181], v[206:209], v[32:35]
	v_mfma_f32_16x16x32_bf16 v[20:23], v[164:167], v[214:217], v[20:23]
	v_mfma_f32_16x16x32_bf16 v[16:19], v[178:181], v[214:217], v[16:19]
	v_mfma_f32_16x16x32_bf16 v[4:7], v[164:167], v[228:231], v[4:7]
	v_mfma_f32_16x16x32_bf16 v[0:3], v[178:181], v[228:231], v[0:3]
	v_mfma_f32_16x16x32_bf16 v[52:55], v[174:177], v[202:205], v[52:55]
	v_mfma_f32_16x16x32_bf16 v[48:51], v[182:185], v[202:205], v[48:51]
	v_mfma_f32_16x16x32_bf16 v[36:39], v[174:177], v[210:213], v[36:39]
	v_mfma_f32_16x16x32_bf16 v[32:35], v[182:185], v[210:213], v[32:35]
	v_mfma_f32_16x16x32_bf16 v[20:23], v[174:177], v[224:227], v[20:23]
	v_mfma_f32_16x16x32_bf16 v[16:19], v[182:185], v[224:227], v[16:19]
	v_mfma_f32_16x16x32_bf16 v[4:7], v[174:177], v[232:235], v[4:7]
	v_mfma_f32_16x16x32_bf16 v[0:3], v[182:185], v[232:235], v[0:3]
	s_setprio 0
	s_barrier
	s_add_i32 s12, s12, 2
	s_addk_i32 s8, 0x100
	s_addk_i32 s9, 0x100
	s_cmp_gt_u32 s12, 61
	s_cbranch_scc0 .LBB0_710
	s_mov_b32 s58, s98
	s_and_b64 vcc, exec, s[2:3]
	s_cbranch_vccz .LBB0_713
	s_barrier

.LBB0_782:
	s_mov_b32 s98, s58
	ds_read_b128 v[16:19], v186
	ds_read_b128 v[20:23], v186 offset:1024
	ds_read_b128 v[24:27], v186 offset:2048
	ds_read_b128 v[28:31], v186 offset:3072
	s_waitcnt lgkmcnt(4)
	ds_read_b128 v[0:3], v186 offset:16384
	ds_read_b128 v[4:7], v186 offset:17408
	ds_read_b128 v[8:11], v186 offset:18432
	ds_read_b128 v[12:15], v186 offset:19456
	s_add_i32 s13, s8, 0xfff80080
	s_cmp_eq_u32 s12, 28
	s_cselect_b32 s15, s52, s13
	s_cselect_b32 s14, s53, s9
	s_add_i32 s13, s15, 0x80
	s_mov_b32 s56, s78
	s_mov_b32 m0, s45
	ds_read_b128 v[174:177], v198
	ds_read_b128 v[178:181], v198 offset:1024
	ds_read_b128 v[200:203], v198 offset:2048
	ds_read_b128 v[204:207], v198 offset:3072
	ds_read_b128 v[208:211], v198 offset:4096
	ds_read_b128 v[212:215], v198 offset:5120
	ds_read_b128 v[224:227], v198 offset:6144
	ds_read_b128 v[228:231], v198 offset:7168
	buffer_load_dwordx4 v165, s[56:59], s8 offen lds
	s_mov_b32 m0, s47
	s_nop 0
	buffer_load_dwordx4 v167, s[56:59], s8 offen lds
	s_waitcnt vmcnt(8)
	s_waitcnt lgkmcnt(0)
	s_barrier
	s_setprio 1
	s_waitcnt lgkmcnt(6)
	v_mfma_f32_16x16x128_f8f6f4 v[156:159], v[16:23], v[174:181], v[156:159]
	v_mfma_f32_16x16x128_f8f6f4 v[152:155], v[24:31], v[174:181], v[152:155]
	s_waitcnt lgkmcnt(4)
	v_mfma_f32_16x16x128_f8f6f4 v[140:143], v[16:23], v[200:207], v[140:143]
	v_mfma_f32_16x16x128_f8f6f4 v[136:139], v[24:31], v[200:207], v[136:139]
	s_waitcnt lgkmcnt(2)
	v_mfma_f32_16x16x128_f8f6f4 v[124:127], v[16:23], v[208:215], v[124:127]
	v_mfma_f32_16x16x128_f8f6f4 v[120:123], v[24:31], v[208:215], v[120:123]
	s_waitcnt lgkmcnt(0)
	v_mfma_f32_16x16x128_f8f6f4 v[108:111], v[16:23], v[224:231], v[108:111]
	v_mfma_f32_16x16x128_f8f6f4 v[104:107], v[24:31], v[224:231], v[104:107]
	s_setprio 0
	s_setprio 1
	v_mfma_f32_16x16x128_f8f6f4 v[148:151], v[0:7], v[174:181], v[148:151]
	v_mfma_f32_16x16x128_f8f6f4 v[144:147], v[8:15], v[174:181], v[144:147]
	v_mfma_f32_16x16x128_f8f6f4 v[132:135], v[0:7], v[200:207], v[132:135]
	v_mfma_f32_16x16x128_f8f6f4 v[128:131], v[8:15], v[200:207], v[128:131]
	v_mfma_f32_16x16x128_f8f6f4 v[116:119], v[0:7], v[208:215], v[116:119]
	v_mfma_f32_16x16x128_f8f6f4 v[112:115], v[8:15], v[208:215], v[112:115]
	v_mfma_f32_16x16x128_f8f6f4 v[100:103], v[0:7], v[224:231], v[100:103]
	v_mfma_f32_16x16x128_f8f6f4 v[96:99], v[8:15], v[224:231], v[96:99]
	s_setprio 0
	s_barrier
	s_cmp_eq_u64 s[40:41], 0
	s_cselect_b32 s99, 28, -1
	s_cmp_eq_u32 s12, s99
	s_cselect_b32 s58, 0, s58
	s_mov_b32 m0, s21
	ds_read_b128 v[174:177], v198 offset:16384
	ds_read_b128 v[178:181], v198 offset:17408
	ds_read_b128 v[200:203], v198 offset:18432
	ds_read_b128 v[204:207], v198 offset:19456
	ds_read_b128 v[208:211], v198 offset:20480
	ds_read_b128 v[212:215], v198 offset:21504
	ds_read_b128 v[224:227], v198 offset:22528
	ds_read_b128 v[228:231], v198 offset:23552
	buffer_load_dwordx4 v166, s[56:59], s14 offen lds
	s_mov_b32 m0, s22
	s_add_i32 s33, s14, 0x80000
	buffer_load_dwordx4 v172, s[56:59], s14 offen lds
	s_mov_b32 m0, s23
	s_nop 0
	buffer_load_dwordx4 v166, s[56:59], s33 offen lds
	s_mov_b32 m0, s24
	s_nop 0
	buffer_load_dwordx4 v172, s[56:59], s33 offen lds
	s_mov_b32 m0, s20
	s_nop 0
	buffer_load_dwordx4 v165, s[56:59], s15 offen lds
	s_mov_b32 m0, s25
	s_nop 0
	buffer_load_dwordx4 v167, s[56:59], s15 offen lds
	s_waitcnt vmcnt(8)
	s_waitcnt lgkmcnt(0)
	s_barrier
	s_setprio 1
	s_waitcnt lgkmcnt(6)
	v_mfma_f32_16x16x128_f8f6f4 v[92:95], v[16:23], v[174:181], v[92:95]
	v_mfma_f32_16x16x128_f8f6f4 v[88:91], v[24:31], v[174:181], v[88:91]
	s_waitcnt lgkmcnt(4)
	v_mfma_f32_16x16x128_f8f6f4 v[76:79], v[16:23], v[200:207], v[76:79]
	v_mfma_f32_16x16x128_f8f6f4 v[72:75], v[24:31], v[200:207], v[72:75]
	s_waitcnt lgkmcnt(2)
	v_mfma_f32_16x16x128_f8f6f4 v[60:63], v[16:23], v[208:215], v[60:63]
	v_mfma_f32_16x16x128_f8f6f4 v[56:59], v[24:31], v[208:215], v[56:59]
	s_waitcnt lgkmcnt(0)
	v_mfma_f32_16x16x128_f8f6f4 v[44:47], v[16:23], v[224:231], v[44:47]
	v_mfma_f32_16x16x128_f8f6f4 v[40:43], v[24:31], v[224:231], v[40:43]
	s_setprio 0
	s_setprio 1
	v_mfma_f32_16x16x128_f8f6f4 v[84:87], v[0:7], v[174:181], v[84:87]
	v_mfma_f32_16x16x128_f8f6f4 v[80:83], v[8:15], v[174:181], v[80:83]
	v_mfma_f32_16x16x128_f8f6f4 v[68:71], v[0:7], v[200:207], v[68:71]
	v_mfma_f32_16x16x128_f8f6f4 v[64:67], v[8:15], v[200:207], v[64:67]
	v_mfma_f32_16x16x128_f8f6f4 v[52:55], v[0:7], v[208:215], v[52:55]
	v_mfma_f32_16x16x128_f8f6f4 v[48:51], v[8:15], v[208:215], v[48:51]
	v_mfma_f32_16x16x128_f8f6f4 v[36:39], v[0:7], v[224:231], v[36:39]
	v_mfma_f32_16x16x128_f8f6f4 v[32:35], v[8:15], v[224:231], v[32:35]
	s_setprio 0
	s_barrier
	ds_read_b128 v[0:3], v186 offset:32768
	ds_read_b128 v[4:7], v186 offset:33792
	ds_read_b128 v[8:11], v186 offset:34816
	ds_read_b128 v[12:15], v186 offset:35840
	ds_read_b128 v[16:19], v186 offset:49152
	ds_read_b128 v[20:23], v186 offset:50176
	ds_read_b128 v[24:27], v186 offset:51200
	ds_read_b128 v[28:31], v186 offset:52224
	s_add_i32 s15, s15, 0x80000
	s_mov_b32 m0, s26
	ds_read_b128 v[174:177], v198 offset:32768
	ds_read_b128 v[178:181], v198 offset:33792
	ds_read_b128 v[200:203], v198 offset:34816
	ds_read_b128 v[204:207], v198 offset:35840
	ds_read_b128 v[208:211], v198 offset:36864
	ds_read_b128 v[212:215], v198 offset:37888
	ds_read_b128 v[224:227], v198 offset:38912
	ds_read_b128 v[228:231], v198 offset:39936
	buffer_load_dwordx4 v165, s[56:59], s15 offen lds
	s_mov_b32 m0, s27
	s_nop 0
	buffer_load_dwordx4 v167, s[56:59], s15 offen lds
	s_waitcnt vmcnt(8)
	s_waitcnt lgkmcnt(0)
	s_barrier
	s_setprio 1
	s_waitcnt lgkmcnt(6)
	v_mfma_f32_16x16x128_f8f6f4 v[156:159], v[0:7], v[174:181], v[156:159]
	v_mfma_f32_16x16x128_f8f6f4 v[152:155], v[8:15], v[174:181], v[152:155]
	s_waitcnt lgkmcnt(4)
	v_mfma_f32_16x16x128_f8f6f4 v[140:143], v[0:7], v[200:207], v[140:143]
	v_mfma_f32_16x16x128_f8f6f4 v[136:139], v[8:15], v[200:207], v[136:139]
	s_waitcnt lgkmcnt(2)
	v_mfma_f32_16x16x128_f8f6f4 v[124:127], v[0:7], v[208:215], v[124:127]
	v_mfma_f32_16x16x128_f8f6f4 v[120:123], v[8:15], v[208:215], v[120:123]
	s_waitcnt lgkmcnt(0)
	v_mfma_f32_16x16x128_f8f6f4 v[108:111], v[0:7], v[224:231], v[108:111]
	v_mfma_f32_16x16x128_f8f6f4 v[104:107], v[8:15], v[224:231], v[104:107]
	s_setprio 0
	s_setprio 1
	v_mfma_f32_16x16x128_f8f6f4 v[148:151], v[16:23], v[174:181], v[148:151]
	v_mfma_f32_16x16x128_f8f6f4 v[144:147], v[24:31], v[174:181], v[144:147]
	v_mfma_f32_16x16x128_f8f6f4 v[132:135], v[16:23], v[200:207], v[132:135]
	v_mfma_f32_16x16x128_f8f6f4 v[128:131], v[24:31], v[200:207], v[128:131]
	v_mfma_f32_16x16x128_f8f6f4 v[116:119], v[16:23], v[208:215], v[116:119]
	v_mfma_f32_16x16x128_f8f6f4 v[112:115], v[24:31], v[208:215], v[112:115]
	v_mfma_f32_16x16x128_f8f6f4 v[100:103], v[16:23], v[224:231], v[100:103]
	v_mfma_f32_16x16x128_f8f6f4 v[96:99], v[24:31], v[224:231], v[96:99]
	s_setprio 0
	s_barrier
	s_mov_b32 m0, s28
	s_add_i32 s15, s14, 0x80
	ds_read_b128 v[174:177], v198 offset:49152
	ds_read_b128 v[178:181], v198 offset:50176
	ds_read_b128 v[200:203], v198 offset:51200
	ds_read_b128 v[204:207], v198 offset:52224
	ds_read_b128 v[208:211], v198 offset:53248
	ds_read_b128 v[212:215], v198 offset:54272
	ds_read_b128 v[224:227], v198 offset:55296
	ds_read_b128 v[228:231], v198 offset:56320
	buffer_load_dwordx4 v166, s[56:59], s15 offen lds
	s_mov_b32 m0, s29
	s_add_i32 s14, s14, 0x80080
	buffer_load_dwordx4 v172, s[56:59], s15 offen lds
	s_mov_b32 m0, s36
	s_nop 0
	buffer_load_dwordx4 v166, s[56:59], s14 offen lds
	s_mov_b32 m0, s37
	s_nop 0
	buffer_load_dwordx4 v172, s[56:59], s14 offen lds
	s_mov_b32 m0, s30
	s_nop 0
	buffer_load_dwordx4 v165, s[56:59], s13 offen lds
	s_mov_b32 m0, s31
	s_nop 0
	buffer_load_dwordx4 v167, s[56:59], s13 offen lds
	s_waitcnt vmcnt(8)
	s_waitcnt lgkmcnt(0)
	s_barrier
	s_setprio 1
	s_waitcnt lgkmcnt(6)
	v_mfma_f32_16x16x128_f8f6f4 v[92:95], v[0:7], v[174:181], v[92:95]
	v_mfma_f32_16x16x128_f8f6f4 v[88:91], v[8:15], v[174:181], v[88:91]
	s_waitcnt lgkmcnt(4)
	v_mfma_f32_16x16x128_f8f6f4 v[76:79], v[0:7], v[200:207], v[76:79]
	v_mfma_f32_16x16x128_f8f6f4 v[72:75], v[8:15], v[200:207], v[72:75]
	s_waitcnt lgkmcnt(2)
	v_mfma_f32_16x16x128_f8f6f4 v[60:63], v[0:7], v[208:215], v[60:63]
	v_mfma_f32_16x16x128_f8f6f4 v[56:59], v[8:15], v[208:215], v[56:59]
	s_waitcnt lgkmcnt(0)
	v_mfma_f32_16x16x128_f8f6f4 v[44:47], v[0:7], v[224:231], v[44:47]
	v_mfma_f32_16x16x128_f8f6f4 v[40:43], v[8:15], v[224:231], v[40:43]
	s_setprio 0
	s_setprio 1
	v_mfma_f32_16x16x128_f8f6f4 v[84:87], v[16:23], v[174:181], v[84:87]
	v_mfma_f32_16x16x128_f8f6f4 v[80:83], v[24:31], v[174:181], v[80:83]
	v_mfma_f32_16x16x128_f8f6f4 v[68:71], v[16:23], v[200:207], v[68:71]
	v_mfma_f32_16x16x128_f8f6f4 v[64:67], v[24:31], v[200:207], v[64:67]
	v_mfma_f32_16x16x128_f8f6f4 v[52:55], v[16:23], v[208:215], v[52:55]
	v_mfma_f32_16x16x128_f8f6f4 v[48:51], v[24:31], v[208:215], v[48:51]
	v_mfma_f32_16x16x128_f8f6f4 v[36:39], v[16:23], v[224:231], v[36:39]
	v_mfma_f32_16x16x128_f8f6f4 v[32:35], v[24:31], v[224:231], v[32:35]
	s_setprio 0
	s_barrier
	s_add_i32 s12, s12, 2
	s_addk_i32 s8, 0x100
	s_addk_i32 s9, 0x100
	s_cmp_gt_u32 s12, 29
	s_cbranch_scc0 .LBB0_782
	s_mov_b32 s58, s98
	s_and_b64 vcc, exec, s[2:3]
	s_cbranch_vccz .LBB0_785
	s_barrier

.LBB0_965:
	s_mov_b32 s98, s58
	ds_read_b128 v[130:133], v204
	ds_read_b128 v[134:137], v204 offset:1024
	ds_read_b128 v[138:141], v204 offset:2048
	ds_read_b128 v[144:147], v204 offset:3072
	ds_read_b128 v[148:151], v204 offset:16384
	ds_read_b128 v[152:155], v204 offset:17408
	ds_read_b128 v[156:159], v204 offset:18432
	ds_read_b128 v[162:165], v204 offset:19456
	s_add_i32 s15, s0, 0xfffc0080
	s_cmp_eq_u32 s14, 12
	s_cselect_b32 s49, s47, s15
	s_cselect_b32 s33, s48, s1
	s_add_i32 s15, s49, 0x80
	s_mov_b32 s56, s78
	s_mov_b32 m0, s37
	ds_read_b128 v[174:177], v205
	ds_read_b128 v[178:181], v205 offset:1024
	ds_read_b128 v[182:185], v205 offset:2048
	ds_read_b128 v[206:209], v205 offset:3072
	ds_read_b128 v[210:213], v205 offset:4096
	ds_read_b128 v[214:217], v205 offset:5120
	ds_read_b128 v[224:227], v205 offset:6144
	ds_read_b128 v[228:231], v205 offset:7168
	buffer_load_dwordx4 v143, s[56:59], s0 offen lds
	s_mov_b32 m0, s42
	s_nop 0
	buffer_load_dwordx4 v198, s[56:59], s0 offen lds
	s_waitcnt vmcnt(8)
	s_waitcnt lgkmcnt(0)
	s_barrier
	s_setprio 1
	s_waitcnt lgkmcnt(7)
	v_mfma_i32_16x16x64_i8 v[124:127], v[130:133], v[174:177], v[124:127]
	v_mfma_i32_16x16x64_i8 v[120:123], v[138:141], v[174:177], v[120:123]
	s_waitcnt lgkmcnt(5)
	v_mfma_i32_16x16x64_i8 v[116:119], v[130:133], v[182:185], v[116:119]
	v_mfma_i32_16x16x64_i8 v[112:115], v[138:141], v[182:185], v[112:115]
	s_waitcnt lgkmcnt(3)
	v_mfma_i32_16x16x64_i8 v[108:111], v[130:133], v[210:213], v[108:111]
	v_mfma_i32_16x16x64_i8 v[104:107], v[138:141], v[210:213], v[104:107]
	s_waitcnt lgkmcnt(1)
	v_mfma_i32_16x16x64_i8 v[100:103], v[130:133], v[224:227], v[100:103]
	v_mfma_i32_16x16x64_i8 v[96:99], v[138:141], v[224:227], v[96:99]
	v_mfma_i32_16x16x64_i8 v[124:127], v[134:137], v[178:181], v[124:127]
	v_mfma_i32_16x16x64_i8 v[120:123], v[144:147], v[178:181], v[120:123]
	v_mfma_i32_16x16x64_i8 v[116:119], v[134:137], v[206:209], v[116:119]
	v_mfma_i32_16x16x64_i8 v[112:115], v[144:147], v[206:209], v[112:115]
	v_mfma_i32_16x16x64_i8 v[108:111], v[134:137], v[214:217], v[108:111]
	v_mfma_i32_16x16x64_i8 v[104:107], v[144:147], v[214:217], v[104:107]
	s_waitcnt lgkmcnt(0)
	v_mfma_i32_16x16x64_i8 v[100:103], v[134:137], v[228:231], v[100:103]
	v_mfma_i32_16x16x64_i8 v[96:99], v[144:147], v[228:231], v[96:99]
	s_setprio 0
	s_setprio 1
	v_mfma_i32_16x16x64_i8 v[92:95], v[148:151], v[174:177], v[92:95]
	v_mfma_i32_16x16x64_i8 v[88:91], v[156:159], v[174:177], v[88:91]
	v_mfma_i32_16x16x64_i8 v[84:87], v[148:151], v[182:185], v[84:87]
	v_mfma_i32_16x16x64_i8 v[80:83], v[156:159], v[182:185], v[80:83]
	v_mfma_i32_16x16x64_i8 v[76:79], v[148:151], v[210:213], v[76:79]
	v_mfma_i32_16x16x64_i8 v[72:75], v[156:159], v[210:213], v[72:75]
	v_mfma_i32_16x16x64_i8 v[68:71], v[148:151], v[224:227], v[68:71]
	v_mfma_i32_16x16x64_i8 v[64:67], v[156:159], v[224:227], v[64:67]
	v_mfma_i32_16x16x64_i8 v[92:95], v[152:155], v[178:181], v[92:95]
	v_mfma_i32_16x16x64_i8 v[88:91], v[162:165], v[178:181], v[88:91]
	v_mfma_i32_16x16x64_i8 v[84:87], v[152:155], v[206:209], v[84:87]
	v_mfma_i32_16x16x64_i8 v[80:83], v[162:165], v[206:209], v[80:83]
	v_mfma_i32_16x16x64_i8 v[76:79], v[152:155], v[214:217], v[76:79]
	v_mfma_i32_16x16x64_i8 v[72:75], v[162:165], v[214:217], v[72:75]
	v_mfma_i32_16x16x64_i8 v[68:71], v[152:155], v[228:231], v[68:71]
	v_mfma_i32_16x16x64_i8 v[64:67], v[162:165], v[228:231], v[64:67]
	s_setprio 0
	s_barrier
	s_cmp_eq_u64 s[40:41], 0
	s_cselect_b32 s99, 12, -1
	s_cmp_eq_u32 s14, s99
	s_cselect_b32 s58, 0, s58
	s_mov_b32 m0, s19
	ds_read_b128 v[174:177], v205 offset:16384
	ds_read_b128 v[178:181], v205 offset:17408
	ds_read_b128 v[182:185], v205 offset:18432
	ds_read_b128 v[206:209], v205 offset:19456
	ds_read_b128 v[210:213], v205 offset:20480
	ds_read_b128 v[214:217], v205 offset:21504
	ds_read_b128 v[224:227], v205 offset:22528
	ds_read_b128 v[228:231], v205 offset:23552
	buffer_load_dwordx4 v161, s[56:59], s33 offen lds
	s_mov_b32 m0, s20
	s_add_i32 s52, s33, 0x40000
	buffer_load_dwordx4 v199, s[56:59], s33 offen lds
	s_mov_b32 m0, s21
	s_nop 0
	buffer_load_dwordx4 v161, s[56:59], s52 offen lds
	s_mov_b32 m0, s22
	s_nop 0
	buffer_load_dwordx4 v199, s[56:59], s52 offen lds
	s_mov_b32 m0, s18
	s_nop 0
	buffer_load_dwordx4 v143, s[56:59], s49 offen lds
	s_mov_b32 m0, s23
	s_nop 0
	buffer_load_dwordx4 v198, s[56:59], s49 offen lds
	s_waitcnt vmcnt(8)
	s_waitcnt lgkmcnt(0)
	s_barrier
	s_setprio 1
	s_waitcnt lgkmcnt(7)
	v_mfma_i32_16x16x64_i8 v[60:63], v[130:133], v[174:177], v[60:63]
	v_mfma_i32_16x16x64_i8 v[56:59], v[138:141], v[174:177], v[56:59]
	s_waitcnt lgkmcnt(5)
	v_mfma_i32_16x16x64_i8 v[52:55], v[130:133], v[182:185], v[52:55]
	v_mfma_i32_16x16x64_i8 v[48:51], v[138:141], v[182:185], v[48:51]
	s_waitcnt lgkmcnt(3)
	v_mfma_i32_16x16x64_i8 v[44:47], v[130:133], v[210:213], v[44:47]
	v_mfma_i32_16x16x64_i8 v[40:43], v[138:141], v[210:213], v[40:43]
	s_waitcnt lgkmcnt(1)
	v_mfma_i32_16x16x64_i8 v[36:39], v[130:133], v[224:227], v[36:39]
	v_mfma_i32_16x16x64_i8 v[32:35], v[138:141], v[224:227], v[32:35]
	v_mfma_i32_16x16x64_i8 v[60:63], v[134:137], v[178:181], v[60:63]
	v_mfma_i32_16x16x64_i8 v[56:59], v[144:147], v[178:181], v[56:59]
	v_mfma_i32_16x16x64_i8 v[52:55], v[134:137], v[206:209], v[52:55]
	v_mfma_i32_16x16x64_i8 v[48:51], v[144:147], v[206:209], v[48:51]
	v_mfma_i32_16x16x64_i8 v[44:47], v[134:137], v[214:217], v[44:47]
	v_mfma_i32_16x16x64_i8 v[40:43], v[144:147], v[214:217], v[40:43]
	s_waitcnt lgkmcnt(0)
	v_mfma_i32_16x16x64_i8 v[36:39], v[134:137], v[228:231], v[36:39]
	v_mfma_i32_16x16x64_i8 v[32:35], v[144:147], v[228:231], v[32:35]
	s_setprio 0
	s_setprio 1
	v_mfma_i32_16x16x64_i8 v[28:31], v[148:151], v[174:177], v[28:31]
	v_mfma_i32_16x16x64_i8 v[24:27], v[156:159], v[174:177], v[24:27]
	v_mfma_i32_16x16x64_i8 v[20:23], v[148:151], v[182:185], v[20:23]
	v_mfma_i32_16x16x64_i8 v[16:19], v[156:159], v[182:185], v[16:19]
	v_mfma_i32_16x16x64_i8 v[12:15], v[148:151], v[210:213], v[12:15]
	v_mfma_i32_16x16x64_i8 v[8:11], v[156:159], v[210:213], v[8:11]
	v_mfma_i32_16x16x64_i8 v[4:7], v[148:151], v[224:227], v[4:7]
	v_mfma_i32_16x16x64_i8 v[0:3], v[156:159], v[224:227], v[0:3]
	v_mfma_i32_16x16x64_i8 v[28:31], v[152:155], v[178:181], v[28:31]
	v_mfma_i32_16x16x64_i8 v[24:27], v[162:165], v[178:181], v[24:27]
	v_mfma_i32_16x16x64_i8 v[20:23], v[152:155], v[206:209], v[20:23]
	v_mfma_i32_16x16x64_i8 v[16:19], v[162:165], v[206:209], v[16:19]
	v_mfma_i32_16x16x64_i8 v[12:15], v[152:155], v[214:217], v[12:15]
	v_mfma_i32_16x16x64_i8 v[8:11], v[162:165], v[214:217], v[8:11]
	v_mfma_i32_16x16x64_i8 v[4:7], v[152:155], v[228:231], v[4:7]
	v_mfma_i32_16x16x64_i8 v[0:3], v[162:165], v[228:231], v[0:3]
	s_setprio 0
	s_barrier
	ds_read_b128 v[130:133], v204 offset:32768
	ds_read_b128 v[134:137], v204 offset:33792
	ds_read_b128 v[138:141], v204 offset:34816
	ds_read_b128 v[144:147], v204 offset:35840
	ds_read_b128 v[148:151], v204 offset:49152
	ds_read_b128 v[152:155], v204 offset:50176
	ds_read_b128 v[156:159], v204 offset:51200
	ds_read_b128 v[162:165], v204 offset:52224
	s_add_i32 s49, s49, 0x40000
	s_mov_b32 m0, s25
	ds_read_b128 v[174:177], v205 offset:32768
	ds_read_b128 v[178:181], v205 offset:33792
	ds_read_b128 v[182:185], v205 offset:34816
	ds_read_b128 v[206:209], v205 offset:35840
	ds_read_b128 v[210:213], v205 offset:36864
	ds_read_b128 v[214:217], v205 offset:37888
	ds_read_b128 v[224:227], v205 offset:38912
	ds_read_b128 v[228:231], v205 offset:39936
	buffer_load_dwordx4 v143, s[56:59], s49 offen lds
	s_mov_b32 m0, s26
	s_nop 0
	buffer_load_dwordx4 v198, s[56:59], s49 offen lds
	s_waitcnt vmcnt(8)
	s_waitcnt lgkmcnt(0)
	s_barrier
	s_setprio 1
	s_waitcnt lgkmcnt(7)
	v_mfma_i32_16x16x64_i8 v[124:127], v[130:133], v[174:177], v[124:127]
	v_mfma_i32_16x16x64_i8 v[120:123], v[138:141], v[174:177], v[120:123]
	s_waitcnt lgkmcnt(5)
	v_mfma_i32_16x16x64_i8 v[116:119], v[130:133], v[182:185], v[116:119]
	v_mfma_i32_16x16x64_i8 v[112:115], v[138:141], v[182:185], v[112:115]
	s_waitcnt lgkmcnt(3)
	v_mfma_i32_16x16x64_i8 v[108:111], v[130:133], v[210:213], v[108:111]
	v_mfma_i32_16x16x64_i8 v[104:107], v[138:141], v[210:213], v[104:107]
	s_waitcnt lgkmcnt(1)
	v_mfma_i32_16x16x64_i8 v[100:103], v[130:133], v[224:227], v[100:103]
	v_mfma_i32_16x16x64_i8 v[96:99], v[138:141], v[224:227], v[96:99]
	v_mfma_i32_16x16x64_i8 v[124:127], v[134:137], v[178:181], v[124:127]
	v_mfma_i32_16x16x64_i8 v[120:123], v[144:147], v[178:181], v[120:123]
	v_mfma_i32_16x16x64_i8 v[116:119], v[134:137], v[206:209], v[116:119]
	v_mfma_i32_16x16x64_i8 v[112:115], v[144:147], v[206:209], v[112:115]
	v_mfma_i32_16x16x64_i8 v[108:111], v[134:137], v[214:217], v[108:111]
	v_mfma_i32_16x16x64_i8 v[104:107], v[144:147], v[214:217], v[104:107]
	s_waitcnt lgkmcnt(0)
	v_mfma_i32_16x16x64_i8 v[100:103], v[134:137], v[228:231], v[100:103]
	v_mfma_i32_16x16x64_i8 v[96:99], v[144:147], v[228:231], v[96:99]
	s_setprio 0
	s_setprio 1
	v_mfma_i32_16x16x64_i8 v[92:95], v[148:151], v[174:177], v[92:95]
	v_mfma_i32_16x16x64_i8 v[88:91], v[156:159], v[174:177], v[88:91]
	v_mfma_i32_16x16x64_i8 v[84:87], v[148:151], v[182:185], v[84:87]
	v_mfma_i32_16x16x64_i8 v[80:83], v[156:159], v[182:185], v[80:83]
	v_mfma_i32_16x16x64_i8 v[76:79], v[148:151], v[210:213], v[76:79]
	v_mfma_i32_16x16x64_i8 v[72:75], v[156:159], v[210:213], v[72:75]
	v_mfma_i32_16x16x64_i8 v[68:71], v[148:151], v[224:227], v[68:71]
	v_mfma_i32_16x16x64_i8 v[64:67], v[156:159], v[224:227], v[64:67]
	v_mfma_i32_16x16x64_i8 v[92:95], v[152:155], v[178:181], v[92:95]
	v_mfma_i32_16x16x64_i8 v[88:91], v[162:165], v[178:181], v[88:91]
	v_mfma_i32_16x16x64_i8 v[84:87], v[152:155], v[206:209], v[84:87]
	v_mfma_i32_16x16x64_i8 v[80:83], v[162:165], v[206:209], v[80:83]
	v_mfma_i32_16x16x64_i8 v[76:79], v[152:155], v[214:217], v[76:79]
	v_mfma_i32_16x16x64_i8 v[72:75], v[162:165], v[214:217], v[72:75]
	v_mfma_i32_16x16x64_i8 v[68:71], v[152:155], v[228:231], v[68:71]
	v_mfma_i32_16x16x64_i8 v[64:67], v[162:165], v[228:231], v[64:67]
	s_setprio 0
	s_barrier
	s_mov_b32 m0, s27
	s_add_i32 s49, s33, 0x80
	ds_read_b128 v[174:177], v205 offset:49152
	ds_read_b128 v[178:181], v205 offset:50176
	ds_read_b128 v[182:185], v205 offset:51200
	ds_read_b128 v[206:209], v205 offset:52224
	ds_read_b128 v[210:213], v205 offset:53248
	ds_read_b128 v[214:217], v205 offset:54272
	ds_read_b128 v[224:227], v205 offset:55296
	ds_read_b128 v[228:231], v205 offset:56320
	buffer_load_dwordx4 v161, s[56:59], s49 offen lds
	s_mov_b32 m0, s28
	s_add_i32 s33, s33, 0x40080
	buffer_load_dwordx4 v199, s[56:59], s49 offen lds
	s_mov_b32 m0, s31
	s_nop 0
	buffer_load_dwordx4 v161, s[56:59], s33 offen lds
	s_mov_b32 m0, s36
	s_nop 0
	buffer_load_dwordx4 v199, s[56:59], s33 offen lds
	s_mov_b32 m0, s29
	s_nop 0
	buffer_load_dwordx4 v143, s[56:59], s15 offen lds
	s_mov_b32 m0, s30
	s_nop 0
	buffer_load_dwordx4 v198, s[56:59], s15 offen lds
	s_waitcnt vmcnt(8)
	s_waitcnt lgkmcnt(0)
	s_barrier
	s_setprio 1
	s_waitcnt lgkmcnt(7)
	v_mfma_i32_16x16x64_i8 v[60:63], v[130:133], v[174:177], v[60:63]
	v_mfma_i32_16x16x64_i8 v[56:59], v[138:141], v[174:177], v[56:59]
	s_waitcnt lgkmcnt(5)
	v_mfma_i32_16x16x64_i8 v[52:55], v[130:133], v[182:185], v[52:55]
	v_mfma_i32_16x16x64_i8 v[48:51], v[138:141], v[182:185], v[48:51]
	s_waitcnt lgkmcnt(3)
	v_mfma_i32_16x16x64_i8 v[44:47], v[130:133], v[210:213], v[44:47]
	v_mfma_i32_16x16x64_i8 v[40:43], v[138:141], v[210:213], v[40:43]
	s_waitcnt lgkmcnt(1)
	v_mfma_i32_16x16x64_i8 v[36:39], v[130:133], v[224:227], v[36:39]
	v_mfma_i32_16x16x64_i8 v[32:35], v[138:141], v[224:227], v[32:35]
	v_mfma_i32_16x16x64_i8 v[60:63], v[134:137], v[178:181], v[60:63]
	v_mfma_i32_16x16x64_i8 v[56:59], v[144:147], v[178:181], v[56:59]
	v_mfma_i32_16x16x64_i8 v[52:55], v[134:137], v[206:209], v[52:55]
	v_mfma_i32_16x16x64_i8 v[48:51], v[144:147], v[206:209], v[48:51]
	v_mfma_i32_16x16x64_i8 v[44:47], v[134:137], v[214:217], v[44:47]
	v_mfma_i32_16x16x64_i8 v[40:43], v[144:147], v[214:217], v[40:43]
	s_waitcnt lgkmcnt(0)
	v_mfma_i32_16x16x64_i8 v[36:39], v[134:137], v[228:231], v[36:39]
	v_mfma_i32_16x16x64_i8 v[32:35], v[144:147], v[228:231], v[32:35]
	s_setprio 0
	s_setprio 1
	v_mfma_i32_16x16x64_i8 v[28:31], v[148:151], v[174:177], v[28:31]
	v_mfma_i32_16x16x64_i8 v[24:27], v[156:159], v[174:177], v[24:27]
	v_mfma_i32_16x16x64_i8 v[20:23], v[148:151], v[182:185], v[20:23]
	v_mfma_i32_16x16x64_i8 v[16:19], v[156:159], v[182:185], v[16:19]
	v_mfma_i32_16x16x64_i8 v[12:15], v[148:151], v[210:213], v[12:15]
	v_mfma_i32_16x16x64_i8 v[8:11], v[156:159], v[210:213], v[8:11]
	v_mfma_i32_16x16x64_i8 v[4:7], v[148:151], v[224:227], v[4:7]
	v_mfma_i32_16x16x64_i8 v[0:3], v[156:159], v[224:227], v[0:3]
	v_mfma_i32_16x16x64_i8 v[28:31], v[152:155], v[178:181], v[28:31]
	v_mfma_i32_16x16x64_i8 v[24:27], v[162:165], v[178:181], v[24:27]
	v_mfma_i32_16x16x64_i8 v[20:23], v[152:155], v[206:209], v[20:23]
	v_mfma_i32_16x16x64_i8 v[16:19], v[162:165], v[206:209], v[16:19]
	v_mfma_i32_16x16x64_i8 v[12:15], v[152:155], v[214:217], v[12:15]
	v_mfma_i32_16x16x64_i8 v[8:11], v[162:165], v[214:217], v[8:11]
	v_mfma_i32_16x16x64_i8 v[4:7], v[152:155], v[228:231], v[4:7]
	v_mfma_i32_16x16x64_i8 v[0:3], v[162:165], v[228:231], v[0:3]
	s_setprio 0
	s_barrier
	s_add_i32 s14, s14, 2
	s_addk_i32 s0, 0x100
	s_addk_i32 s1, 0x100
	s_cmp_gt_u32 s14, 13
	s_cbranch_scc0 .LBB0_965
	s_mov_b32 s58, s98
	s_and_b64 vcc, exec, s[16:17]
	s_cbranch_vccz .LBB0_968
	s_barrier

.LBB0_983:
	s_mov_b32 s98, s58
	ds_read_b128 v[16:19], v205
	ds_read_b128 v[20:23], v205 offset:1024
	ds_read_b128 v[24:27], v205 offset:2048
	ds_read_b128 v[28:31], v205 offset:3072
	ds_read_b128 v[0:3], v205 offset:16384
	ds_read_b128 v[4:7], v205 offset:17408
	ds_read_b128 v[8:11], v205 offset:18432
	ds_read_b128 v[12:15], v205 offset:19456
	s_add_i32 s14, s0, 0xfffc0080
	s_cmp_eq_u32 s13, 12
	s_cselect_b32 s33, s47, s14
	s_cselect_b32 s15, s48, s1
	s_add_i32 s14, s33, 0x80
	s_mov_b32 s56, s78
	s_mov_b32 m0, s41
	ds_read_b128 v[174:177], v206
	ds_read_b128 v[178:181], v206 offset:1024
	ds_read_b128 v[208:211], v206 offset:2048
	ds_read_b128 v[212:215], v206 offset:3072
	ds_read_b128 v[224:227], v206 offset:4096
	ds_read_b128 v[228:231], v206 offset:5120
	ds_read_b128 v[232:235], v206 offset:6144
	ds_read_b128 v[236:239], v206 offset:7168
	buffer_load_dwordx4 v182, s[56:59], s0 offen lds
	s_mov_b32 m0, s42
	s_nop 0
	buffer_load_dwordx4 v184, s[56:59], s0 offen lds
	s_waitcnt vmcnt(8)
	s_waitcnt lgkmcnt(0)
	s_barrier
	s_setprio 1
	s_waitcnt lgkmcnt(6)
	v_mfma_f32_16x16x128_f8f6f4 v[156:159], v[16:23], v[174:181], v[156:159]
	v_mfma_f32_16x16x128_f8f6f4 v[148:151], v[24:31], v[174:181], v[148:151]
	s_waitcnt lgkmcnt(4)
	v_mfma_f32_16x16x128_f8f6f4 v[140:143], v[16:23], v[208:215], v[140:143]
	v_mfma_f32_16x16x128_f8f6f4 v[132:135], v[24:31], v[208:215], v[132:135]
	s_waitcnt lgkmcnt(2)
	v_mfma_f32_16x16x128_f8f6f4 v[124:127], v[16:23], v[224:231], v[124:127]
	v_mfma_f32_16x16x128_f8f6f4 v[116:119], v[24:31], v[224:231], v[116:119]
	s_waitcnt lgkmcnt(0)
	v_mfma_f32_16x16x128_f8f6f4 v[108:111], v[16:23], v[232:239], v[108:111]
	v_mfma_f32_16x16x128_f8f6f4 v[100:103], v[24:31], v[232:239], v[100:103]
	s_setprio 0
	s_setprio 1
	v_mfma_f32_16x16x128_f8f6f4 v[152:155], v[0:7], v[174:181], v[152:155]
	v_mfma_f32_16x16x128_f8f6f4 v[144:147], v[8:15], v[174:181], v[144:147]
	v_mfma_f32_16x16x128_f8f6f4 v[136:139], v[0:7], v[208:215], v[136:139]
	v_mfma_f32_16x16x128_f8f6f4 v[128:131], v[8:15], v[208:215], v[128:131]
	v_mfma_f32_16x16x128_f8f6f4 v[120:123], v[0:7], v[224:231], v[120:123]
	v_mfma_f32_16x16x128_f8f6f4 v[112:115], v[8:15], v[224:231], v[112:115]
	v_mfma_f32_16x16x128_f8f6f4 v[104:107], v[0:7], v[232:239], v[104:107]
	v_mfma_f32_16x16x128_f8f6f4 v[96:99], v[8:15], v[232:239], v[96:99]
	s_setprio 0
	s_barrier
	s_cmp_eq_u64 s[38:39], 0
	s_cselect_b32 s99, 12, -1
	s_cmp_eq_u32 s13, s99
	s_cselect_b32 s58, 0, s58
	s_mov_b32 m0, s9
	ds_read_b128 v[174:177], v206 offset:16384
	ds_read_b128 v[178:181], v206 offset:17408
	ds_read_b128 v[208:211], v206 offset:18432
	ds_read_b128 v[212:215], v206 offset:19456
	ds_read_b128 v[224:227], v206 offset:20480
	ds_read_b128 v[228:231], v206 offset:21504
	ds_read_b128 v[232:235], v206 offset:22528
	ds_read_b128 v[236:239], v206 offset:23552
	buffer_load_dwordx4 v183, s[56:59], s15 offen lds
	s_mov_b32 m0, s10
	s_add_i32 s49, s15, 0x40000
	buffer_load_dwordx4 v185, s[56:59], s15 offen lds
	s_mov_b32 m0, s11
	s_nop 0
	buffer_load_dwordx4 v183, s[56:59], s49 offen lds
	s_mov_b32 m0, s25
	s_nop 0
	buffer_load_dwordx4 v185, s[56:59], s49 offen lds
	s_mov_b32 m0, s8
	s_nop 0
	buffer_load_dwordx4 v182, s[56:59], s33 offen lds
	s_mov_b32 m0, s26
	s_nop 0
	buffer_load_dwordx4 v184, s[56:59], s33 offen lds
	s_waitcnt vmcnt(8)
	s_waitcnt lgkmcnt(0)
	s_barrier
	s_setprio 1
	s_waitcnt lgkmcnt(6)
	v_mfma_f32_16x16x128_f8f6f4 v[92:95], v[16:23], v[174:181], v[92:95]
	v_mfma_f32_16x16x128_f8f6f4 v[84:87], v[24:31], v[174:181], v[84:87]
	s_waitcnt lgkmcnt(4)
	v_mfma_f32_16x16x128_f8f6f4 v[76:79], v[16:23], v[208:215], v[76:79]
	v_mfma_f32_16x16x128_f8f6f4 v[68:71], v[24:31], v[208:215], v[68:71]
	s_waitcnt lgkmcnt(2)
	v_mfma_f32_16x16x128_f8f6f4 v[60:63], v[16:23], v[224:231], v[60:63]
	v_mfma_f32_16x16x128_f8f6f4 v[52:55], v[24:31], v[224:231], v[52:55]
	s_waitcnt lgkmcnt(0)
	v_mfma_f32_16x16x128_f8f6f4 v[44:47], v[16:23], v[232:239], v[44:47]
	v_mfma_f32_16x16x128_f8f6f4 v[36:39], v[24:31], v[232:239], v[36:39]
	s_setprio 0
	s_setprio 1
	v_mfma_f32_16x16x128_f8f6f4 v[88:91], v[0:7], v[174:181], v[88:91]
	v_mfma_f32_16x16x128_f8f6f4 v[80:83], v[8:15], v[174:181], v[80:83]
	v_mfma_f32_16x16x128_f8f6f4 v[72:75], v[0:7], v[208:215], v[72:75]
	v_mfma_f32_16x16x128_f8f6f4 v[64:67], v[8:15], v[208:215], v[64:67]
	v_mfma_f32_16x16x128_f8f6f4 v[56:59], v[0:7], v[224:231], v[56:59]
	v_mfma_f32_16x16x128_f8f6f4 v[48:51], v[8:15], v[224:231], v[48:51]
	v_mfma_f32_16x16x128_f8f6f4 v[40:43], v[0:7], v[232:239], v[40:43]
	v_mfma_f32_16x16x128_f8f6f4 v[32:35], v[8:15], v[232:239], v[32:35]
	s_setprio 0
	s_barrier
	ds_read_b128 v[0:3], v205 offset:32768
	ds_read_b128 v[4:7], v205 offset:33792
	ds_read_b128 v[8:11], v205 offset:34816
	ds_read_b128 v[12:15], v205 offset:35840
	ds_read_b128 v[16:19], v205 offset:49152
	ds_read_b128 v[20:23], v205 offset:50176
	ds_read_b128 v[24:27], v205 offset:51200
	ds_read_b128 v[28:31], v205 offset:52224
	s_add_i32 s33, s33, 0x40000
	s_mov_b32 m0, s27
	ds_read_b128 v[174:177], v206 offset:32768
	ds_read_b128 v[178:181], v206 offset:33792
	ds_read_b128 v[208:211], v206 offset:34816
	ds_read_b128 v[212:215], v206 offset:35840
	ds_read_b128 v[224:227], v206 offset:36864
	ds_read_b128 v[228:231], v206 offset:37888
	ds_read_b128 v[232:235], v206 offset:38912
	ds_read_b128 v[236:239], v206 offset:39936
	buffer_load_dwordx4 v182, s[56:59], s33 offen lds
	s_mov_b32 m0, s28
	s_nop 0
	buffer_load_dwordx4 v184, s[56:59], s33 offen lds
	s_waitcnt vmcnt(8)
	s_waitcnt lgkmcnt(0)
	s_barrier
	s_setprio 1
	s_waitcnt lgkmcnt(6)
	v_mfma_f32_16x16x128_f8f6f4 v[156:159], v[0:7], v[174:181], v[156:159]
	v_mfma_f32_16x16x128_f8f6f4 v[148:151], v[8:15], v[174:181], v[148:151]
	s_waitcnt lgkmcnt(4)
	v_mfma_f32_16x16x128_f8f6f4 v[140:143], v[0:7], v[208:215], v[140:143]
	v_mfma_f32_16x16x128_f8f6f4 v[132:135], v[8:15], v[208:215], v[132:135]
	s_waitcnt lgkmcnt(2)
	v_mfma_f32_16x16x128_f8f6f4 v[124:127], v[0:7], v[224:231], v[124:127]
	v_mfma_f32_16x16x128_f8f6f4 v[116:119], v[8:15], v[224:231], v[116:119]
	s_waitcnt lgkmcnt(0)
	v_mfma_f32_16x16x128_f8f6f4 v[108:111], v[0:7], v[232:239], v[108:111]
	v_mfma_f32_16x16x128_f8f6f4 v[100:103], v[8:15], v[232:239], v[100:103]
	s_setprio 0
	s_setprio 1
	v_mfma_f32_16x16x128_f8f6f4 v[152:155], v[16:23], v[174:181], v[152:155]
	v_mfma_f32_16x16x128_f8f6f4 v[144:147], v[24:31], v[174:181], v[144:147]
	v_mfma_f32_16x16x128_f8f6f4 v[136:139], v[16:23], v[208:215], v[136:139]
	v_mfma_f32_16x16x128_f8f6f4 v[128:131], v[24:31], v[208:215], v[128:131]
	v_mfma_f32_16x16x128_f8f6f4 v[120:123], v[16:23], v[224:231], v[120:123]
	v_mfma_f32_16x16x128_f8f6f4 v[112:115], v[24:31], v[224:231], v[112:115]
	v_mfma_f32_16x16x128_f8f6f4 v[104:107], v[16:23], v[232:239], v[104:107]
	v_mfma_f32_16x16x128_f8f6f4 v[96:99], v[24:31], v[232:239], v[96:99]
	s_setprio 0
	s_barrier
	s_mov_b32 m0, s29
	s_add_i32 s33, s15, 0x80
	ds_read_b128 v[174:177], v206 offset:49152
	ds_read_b128 v[178:181], v206 offset:50176
	ds_read_b128 v[208:211], v206 offset:51200
	ds_read_b128 v[212:215], v206 offset:52224
	ds_read_b128 v[224:227], v206 offset:53248
	ds_read_b128 v[228:231], v206 offset:54272
	ds_read_b128 v[232:235], v206 offset:55296
	ds_read_b128 v[236:239], v206 offset:56320
	buffer_load_dwordx4 v183, s[56:59], s33 offen lds
	s_mov_b32 m0, s30
	s_add_i32 s15, s15, 0x40080
	buffer_load_dwordx4 v185, s[56:59], s33 offen lds
	s_mov_b32 m0, s37
	s_nop 0
	buffer_load_dwordx4 v183, s[56:59], s15 offen lds
	s_mov_b32 m0, s40
	s_nop 0
	buffer_load_dwordx4 v185, s[56:59], s15 offen lds
	s_mov_b32 m0, s31
	s_nop 0
	buffer_load_dwordx4 v182, s[56:59], s14 offen lds
	s_mov_b32 m0, s36
	s_nop 0
	buffer_load_dwordx4 v184, s[56:59], s14 offen lds
	s_waitcnt vmcnt(8)
	s_waitcnt lgkmcnt(0)
	s_barrier
	s_setprio 1
	s_waitcnt lgkmcnt(6)
	v_mfma_f32_16x16x128_f8f6f4 v[92:95], v[0:7], v[174:181], v[92:95]
	v_mfma_f32_16x16x128_f8f6f4 v[84:87], v[8:15], v[174:181], v[84:87]
	s_waitcnt lgkmcnt(4)
	v_mfma_f32_16x16x128_f8f6f4 v[76:79], v[0:7], v[208:215], v[76:79]
	v_mfma_f32_16x16x128_f8f6f4 v[68:71], v[8:15], v[208:215], v[68:71]
	s_waitcnt lgkmcnt(2)
	v_mfma_f32_16x16x128_f8f6f4 v[60:63], v[0:7], v[224:231], v[60:63]
	v_mfma_f32_16x16x128_f8f6f4 v[52:55], v[8:15], v[224:231], v[52:55]
	s_waitcnt lgkmcnt(0)
	v_mfma_f32_16x16x128_f8f6f4 v[44:47], v[0:7], v[232:239], v[44:47]
	v_mfma_f32_16x16x128_f8f6f4 v[36:39], v[8:15], v[232:239], v[36:39]
	s_setprio 0
	s_setprio 1
	v_mfma_f32_16x16x128_f8f6f4 v[88:91], v[16:23], v[174:181], v[88:91]
	v_mfma_f32_16x16x128_f8f6f4 v[80:83], v[24:31], v[174:181], v[80:83]
	v_mfma_f32_16x16x128_f8f6f4 v[72:75], v[16:23], v[208:215], v[72:75]
	v_mfma_f32_16x16x128_f8f6f4 v[64:67], v[24:31], v[208:215], v[64:67]
	v_mfma_f32_16x16x128_f8f6f4 v[56:59], v[16:23], v[224:231], v[56:59]
	v_mfma_f32_16x16x128_f8f6f4 v[48:51], v[24:31], v[224:231], v[48:51]
	v_mfma_f32_16x16x128_f8f6f4 v[40:43], v[16:23], v[232:239], v[40:43]
	v_mfma_f32_16x16x128_f8f6f4 v[32:35], v[24:31], v[232:239], v[32:35]
	s_setprio 0
	s_barrier
	s_add_i32 s13, s13, 2
	s_addk_i32 s0, 0x100
	s_addk_i32 s1, 0x100
	s_cmp_gt_u32 s13, 13
	s_cbranch_scc0 .LBB0_983
	s_mov_b32 s58, s98
	s_and_b64 vcc, exec, s[22:23]
	s_cbranch_vccz .LBB0_986
	s_barrier

.LBB0_1158:
	s_mov_b32 s98, s58
	ds_read_b128 v[16:19], v182
	ds_read_b128 v[20:23], v182 offset:1024
	ds_read_b128 v[24:27], v182 offset:2048
	ds_read_b128 v[28:31], v182 offset:3072
	s_waitcnt lgkmcnt(4)
	ds_read_b128 v[0:3], v182 offset:16384
	ds_read_b128 v[4:7], v182 offset:17408
	ds_read_b128 v[8:11], v182 offset:18432
	ds_read_b128 v[12:15], v182 offset:19456
	s_add_i32 s13, s8, 0xfff50080
	s_cmp_eq_u32 s12, 40
	s_cselect_b32 s15, s42, s13
	s_cselect_b32 s14, s43, s9
	s_add_i32 s13, s15, 0x80
	s_mov_b32 s56, s78
	s_mov_b32 m0, s31
	ds_read_b128 v[174:177], v183
	ds_read_b128 v[178:181], v183 offset:1024
	ds_read_b128 v[198:201], v183 offset:2048
	ds_read_b128 v[202:205], v183 offset:3072
	ds_read_b128 v[206:209], v183 offset:4096
	ds_read_b128 v[210:213], v183 offset:5120
	ds_read_b128 v[224:227], v183 offset:6144
	ds_read_b128 v[228:231], v183 offset:7168
	buffer_load_dwordx4 v160, s[56:59], s8 offen lds
	s_mov_b32 m0, s35
	s_nop 0
	buffer_load_dwordx4 v162, s[56:59], s8 offen lds
	s_waitcnt vmcnt(8)
	s_waitcnt lgkmcnt(0)
	s_barrier
	s_setprio 1
	s_waitcnt lgkmcnt(6)
	v_mfma_f32_16x16x128_f8f6f4 v[156:159], v[16:23], v[174:181], v[156:159]
	v_mfma_f32_16x16x128_f8f6f4 v[152:155], v[24:31], v[174:181], v[152:155]
	s_waitcnt lgkmcnt(4)
	v_mfma_f32_16x16x128_f8f6f4 v[140:143], v[16:23], v[198:205], v[140:143]
	v_mfma_f32_16x16x128_f8f6f4 v[136:139], v[24:31], v[198:205], v[136:139]
	s_waitcnt lgkmcnt(2)
	v_mfma_f32_16x16x128_f8f6f4 v[124:127], v[16:23], v[206:213], v[124:127]
	v_mfma_f32_16x16x128_f8f6f4 v[120:123], v[24:31], v[206:213], v[120:123]
	s_waitcnt lgkmcnt(0)
	v_mfma_f32_16x16x128_f8f6f4 v[108:111], v[16:23], v[224:231], v[108:111]
	v_mfma_f32_16x16x128_f8f6f4 v[104:107], v[24:31], v[224:231], v[104:107]
	s_setprio 0
	s_setprio 1
	v_mfma_f32_16x16x128_f8f6f4 v[148:151], v[0:7], v[174:181], v[148:151]
	v_mfma_f32_16x16x128_f8f6f4 v[144:147], v[8:15], v[174:181], v[144:147]
	v_mfma_f32_16x16x128_f8f6f4 v[132:135], v[0:7], v[198:205], v[132:135]
	v_mfma_f32_16x16x128_f8f6f4 v[128:131], v[8:15], v[198:205], v[128:131]
	v_mfma_f32_16x16x128_f8f6f4 v[116:119], v[0:7], v[206:213], v[116:119]
	v_mfma_f32_16x16x128_f8f6f4 v[112:115], v[8:15], v[206:213], v[112:115]
	v_mfma_f32_16x16x128_f8f6f4 v[100:103], v[0:7], v[224:231], v[100:103]
	v_mfma_f32_16x16x128_f8f6f4 v[96:99], v[8:15], v[224:231], v[96:99]
	s_setprio 0
	s_barrier
	s_cmp_eq_u64 s[40:41], 0
	s_cselect_b32 s99, 40, -1
	s_cmp_eq_u32 s12, s99
	s_cselect_b32 s58, 0, s58
	s_mov_b32 m0, s18
	ds_read_b128 v[174:177], v183 offset:16384
	ds_read_b128 v[178:181], v183 offset:17408
	ds_read_b128 v[198:201], v183 offset:18432
	ds_read_b128 v[202:205], v183 offset:19456
	ds_read_b128 v[206:209], v183 offset:20480
	ds_read_b128 v[210:213], v183 offset:21504
	ds_read_b128 v[224:227], v183 offset:22528
	ds_read_b128 v[228:231], v183 offset:23552
	buffer_load_dwordx4 v161, s[56:59], s14 offen lds
	s_mov_b32 m0, s19
	s_add_i32 s33, s14, 0xb0000
	buffer_load_dwordx4 v163, s[56:59], s14 offen lds
	s_mov_b32 m0, s20
	s_nop 0
	buffer_load_dwordx4 v161, s[56:59], s33 offen lds
	s_mov_b32 m0, s21
	s_nop 0
	buffer_load_dwordx4 v163, s[56:59], s33 offen lds
	s_mov_b32 m0, s7
	s_nop 0
	buffer_load_dwordx4 v160, s[56:59], s15 offen lds
	s_mov_b32 m0, s22
	s_nop 0
	buffer_load_dwordx4 v162, s[56:59], s15 offen lds
	s_waitcnt vmcnt(8)
	s_waitcnt lgkmcnt(0)
	s_barrier
	s_setprio 1
	s_waitcnt lgkmcnt(6)
	v_mfma_f32_16x16x128_f8f6f4 v[92:95], v[16:23], v[174:181], v[92:95]
	v_mfma_f32_16x16x128_f8f6f4 v[88:91], v[24:31], v[174:181], v[88:91]
	s_waitcnt lgkmcnt(4)
	v_mfma_f32_16x16x128_f8f6f4 v[76:79], v[16:23], v[198:205], v[76:79]
	v_mfma_f32_16x16x128_f8f6f4 v[72:75], v[24:31], v[198:205], v[72:75]
	s_waitcnt lgkmcnt(2)
	v_mfma_f32_16x16x128_f8f6f4 v[60:63], v[16:23], v[206:213], v[60:63]
	v_mfma_f32_16x16x128_f8f6f4 v[56:59], v[24:31], v[206:213], v[56:59]
	s_waitcnt lgkmcnt(0)
	v_mfma_f32_16x16x128_f8f6f4 v[44:47], v[16:23], v[224:231], v[44:47]
	v_mfma_f32_16x16x128_f8f6f4 v[40:43], v[24:31], v[224:231], v[40:43]
	s_setprio 0
	s_setprio 1
	v_mfma_f32_16x16x128_f8f6f4 v[84:87], v[0:7], v[174:181], v[84:87]
	v_mfma_f32_16x16x128_f8f6f4 v[80:83], v[8:15], v[174:181], v[80:83]
	v_mfma_f32_16x16x128_f8f6f4 v[68:71], v[0:7], v[198:205], v[68:71]
	v_mfma_f32_16x16x128_f8f6f4 v[64:67], v[8:15], v[198:205], v[64:67]
	v_mfma_f32_16x16x128_f8f6f4 v[52:55], v[0:7], v[206:213], v[52:55]
	v_mfma_f32_16x16x128_f8f6f4 v[48:51], v[8:15], v[206:213], v[48:51]
	v_mfma_f32_16x16x128_f8f6f4 v[36:39], v[0:7], v[224:231], v[36:39]
	v_mfma_f32_16x16x128_f8f6f4 v[32:35], v[8:15], v[224:231], v[32:35]
	s_setprio 0
	s_barrier
	ds_read_b128 v[0:3], v182 offset:32768
	ds_read_b128 v[4:7], v182 offset:33792
	ds_read_b128 v[8:11], v182 offset:34816
	ds_read_b128 v[12:15], v182 offset:35840
	ds_read_b128 v[16:19], v182 offset:49152
	ds_read_b128 v[20:23], v182 offset:50176
	ds_read_b128 v[24:27], v182 offset:51200
	ds_read_b128 v[28:31], v182 offset:52224
	s_add_i32 s15, s15, 0xb0000
	s_mov_b32 m0, s23
	ds_read_b128 v[174:177], v183 offset:32768
	ds_read_b128 v[178:181], v183 offset:33792
	ds_read_b128 v[198:201], v183 offset:34816
	ds_read_b128 v[202:205], v183 offset:35840
	ds_read_b128 v[206:209], v183 offset:36864
	ds_read_b128 v[210:213], v183 offset:37888
	ds_read_b128 v[224:227], v183 offset:38912
	ds_read_b128 v[228:231], v183 offset:39936
	buffer_load_dwordx4 v160, s[56:59], s15 offen lds
	s_mov_b32 m0, s24
	s_nop 0
	buffer_load_dwordx4 v162, s[56:59], s15 offen lds
	s_waitcnt vmcnt(8)
	s_waitcnt lgkmcnt(0)
	s_barrier
	s_setprio 1
	s_waitcnt lgkmcnt(6)
	v_mfma_f32_16x16x128_f8f6f4 v[156:159], v[0:7], v[174:181], v[156:159]
	v_mfma_f32_16x16x128_f8f6f4 v[152:155], v[8:15], v[174:181], v[152:155]
	s_waitcnt lgkmcnt(4)
	v_mfma_f32_16x16x128_f8f6f4 v[140:143], v[0:7], v[198:205], v[140:143]
	v_mfma_f32_16x16x128_f8f6f4 v[136:139], v[8:15], v[198:205], v[136:139]
	s_waitcnt lgkmcnt(2)
	v_mfma_f32_16x16x128_f8f6f4 v[124:127], v[0:7], v[206:213], v[124:127]
	v_mfma_f32_16x16x128_f8f6f4 v[120:123], v[8:15], v[206:213], v[120:123]
	s_waitcnt lgkmcnt(0)
	v_mfma_f32_16x16x128_f8f6f4 v[108:111], v[0:7], v[224:231], v[108:111]
	v_mfma_f32_16x16x128_f8f6f4 v[104:107], v[8:15], v[224:231], v[104:107]
	s_setprio 0
	s_setprio 1
	v_mfma_f32_16x16x128_f8f6f4 v[148:151], v[16:23], v[174:181], v[148:151]
	v_mfma_f32_16x16x128_f8f6f4 v[144:147], v[24:31], v[174:181], v[144:147]
	v_mfma_f32_16x16x128_f8f6f4 v[132:135], v[16:23], v[198:205], v[132:135]
	v_mfma_f32_16x16x128_f8f6f4 v[128:131], v[24:31], v[198:205], v[128:131]
	v_mfma_f32_16x16x128_f8f6f4 v[116:119], v[16:23], v[206:213], v[116:119]
	v_mfma_f32_16x16x128_f8f6f4 v[112:115], v[24:31], v[206:213], v[112:115]
	v_mfma_f32_16x16x128_f8f6f4 v[100:103], v[16:23], v[224:231], v[100:103]
	v_mfma_f32_16x16x128_f8f6f4 v[96:99], v[24:31], v[224:231], v[96:99]
	s_setprio 0
	s_barrier
	s_mov_b32 m0, s25
	s_add_i32 s15, s14, 0x80
	ds_read_b128 v[174:177], v183 offset:49152
	ds_read_b128 v[178:181], v183 offset:50176
	ds_read_b128 v[198:201], v183 offset:51200
	ds_read_b128 v[202:205], v183 offset:52224
	ds_read_b128 v[206:209], v183 offset:53248
	ds_read_b128 v[210:213], v183 offset:54272
	ds_read_b128 v[224:227], v183 offset:55296
	ds_read_b128 v[228:231], v183 offset:56320
	buffer_load_dwordx4 v161, s[56:59], s15 offen lds
	s_mov_b32 m0, s26
	s_add_i32 s14, s14, 0xb0080
	buffer_load_dwordx4 v163, s[56:59], s15 offen lds
	s_mov_b32 m0, s29
	s_nop 0
	buffer_load_dwordx4 v161, s[56:59], s14 offen lds
	s_mov_b32 m0, s30
	s_nop 0
	buffer_load_dwordx4 v163, s[56:59], s14 offen lds
	s_mov_b32 m0, s27
	s_nop 0
	buffer_load_dwordx4 v160, s[56:59], s13 offen lds
	s_mov_b32 m0, s28
	s_nop 0
	buffer_load_dwordx4 v162, s[56:59], s13 offen lds
	s_waitcnt vmcnt(8)
	s_waitcnt lgkmcnt(0)
	s_barrier
	s_setprio 1
	s_waitcnt lgkmcnt(6)
	v_mfma_f32_16x16x128_f8f6f4 v[92:95], v[0:7], v[174:181], v[92:95]
	v_mfma_f32_16x16x128_f8f6f4 v[88:91], v[8:15], v[174:181], v[88:91]
	s_waitcnt lgkmcnt(4)
	v_mfma_f32_16x16x128_f8f6f4 v[76:79], v[0:7], v[198:205], v[76:79]
	v_mfma_f32_16x16x128_f8f6f4 v[72:75], v[8:15], v[198:205], v[72:75]
	s_waitcnt lgkmcnt(2)
	v_mfma_f32_16x16x128_f8f6f4 v[60:63], v[0:7], v[206:213], v[60:63]
	v_mfma_f32_16x16x128_f8f6f4 v[56:59], v[8:15], v[206:213], v[56:59]
	s_waitcnt lgkmcnt(0)
	v_mfma_f32_16x16x128_f8f6f4 v[44:47], v[0:7], v[224:231], v[44:47]
	v_mfma_f32_16x16x128_f8f6f4 v[40:43], v[8:15], v[224:231], v[40:43]
	s_setprio 0
	s_setprio 1
	v_mfma_f32_16x16x128_f8f6f4 v[84:87], v[16:23], v[174:181], v[84:87]
	v_mfma_f32_16x16x128_f8f6f4 v[80:83], v[24:31], v[174:181], v[80:83]
	v_mfma_f32_16x16x128_f8f6f4 v[68:71], v[16:23], v[198:205], v[68:71]
	v_mfma_f32_16x16x128_f8f6f4 v[64:67], v[24:31], v[198:205], v[64:67]
	v_mfma_f32_16x16x128_f8f6f4 v[52:55], v[16:23], v[206:213], v[52:55]
	v_mfma_f32_16x16x128_f8f6f4 v[48:51], v[24:31], v[206:213], v[48:51]
	v_mfma_f32_16x16x128_f8f6f4 v[36:39], v[16:23], v[224:231], v[36:39]
	v_mfma_f32_16x16x128_f8f6f4 v[32:35], v[24:31], v[224:231], v[32:35]
	s_setprio 0
	s_barrier
	s_add_i32 s12, s12, 2
	s_addk_i32 s8, 0x100
	s_addk_i32 s9, 0x100
	s_cmp_gt_u32 s12, 41
	s_cbranch_scc0 .LBB0_1158
	s_mov_b32 s58, s98
	s_and_b64 vcc, exec, s[2:3]
	s_cbranch_vccz .LBB0_1161
	s_barrier

.LBB0_1238:
	s_mov_b32 s98, s58
	ds_read_b128 v[142:145], v140
	ds_read_b128 v[146:149], v140 offset:1024
	ds_read_b128 v[150:153], v140 offset:2048
	ds_read_b128 v[154:157], v140 offset:3072
	ds_read_b128 v[158:161], v140 offset:16384
	ds_read_b128 v[162:165], v140 offset:17408
	ds_read_b128 v[174:177], v140 offset:18432
	ds_read_b128 v[178:181], v140 offset:19456
	s_add_i32 s40, s10, 0xfff80080
	s_cmp_eq_u32 s37, 4
	s_cselect_b32 s42, s35, s40
	s_cselect_b32 s41, s36, s11
	s_add_i32 s40, s42, 0x80
	s_mov_b32 s56, s78
	s_mov_b32 m0, s28
	ds_read_b128 v[182:185], v141
	ds_read_b128 v[198:201], v141 offset:1024
	ds_read_b128 v[202:205], v141 offset:2048
	ds_read_b128 v[206:209], v141 offset:3072
	ds_read_b128 v[210:213], v141 offset:4096
	ds_read_b128 v[214:217], v141 offset:5120
	ds_read_b128 v[224:227], v141 offset:6144
	ds_read_b128 v[228:231], v141 offset:7168
	buffer_load_dwordx4 v128, s[56:59], s10 offen lds
	s_mov_b32 m0, s29
	s_nop 0
	buffer_load_dwordx4 v130, s[56:59], s10 offen lds
	s_waitcnt vmcnt(8)
	s_waitcnt lgkmcnt(0)
	s_barrier
	s_setprio 1
	s_waitcnt lgkmcnt(7)
	v_mfma_f32_16x16x32_bf16 v[124:127], v[142:145], v[182:185], v[124:127]
	v_mfma_f32_16x16x32_bf16 v[120:123], v[150:153], v[182:185], v[120:123]
	s_waitcnt lgkmcnt(5)
	v_mfma_f32_16x16x32_bf16 v[116:119], v[142:145], v[202:205], v[116:119]
	v_mfma_f32_16x16x32_bf16 v[108:111], v[150:153], v[202:205], v[108:111]
	s_waitcnt lgkmcnt(3)
	v_mfma_f32_16x16x32_bf16 v[100:103], v[142:145], v[210:213], v[100:103]
	v_mfma_f32_16x16x32_bf16 v[92:95], v[150:153], v[210:213], v[92:95]
	s_waitcnt lgkmcnt(1)
	v_mfma_f32_16x16x32_bf16 v[84:87], v[142:145], v[224:227], v[84:87]
	v_mfma_f32_16x16x32_bf16 v[76:79], v[150:153], v[224:227], v[76:79]
	v_mfma_f32_16x16x32_bf16 v[124:127], v[146:149], v[198:201], v[124:127]
	v_mfma_f32_16x16x32_bf16 v[120:123], v[154:157], v[198:201], v[120:123]
	v_mfma_f32_16x16x32_bf16 v[116:119], v[146:149], v[206:209], v[116:119]
	v_mfma_f32_16x16x32_bf16 v[108:111], v[154:157], v[206:209], v[108:111]
	v_mfma_f32_16x16x32_bf16 v[100:103], v[146:149], v[214:217], v[100:103]
	v_mfma_f32_16x16x32_bf16 v[92:95], v[154:157], v[214:217], v[92:95]
	s_waitcnt lgkmcnt(0)
	v_mfma_f32_16x16x32_bf16 v[84:87], v[146:149], v[228:231], v[84:87]
	v_mfma_f32_16x16x32_bf16 v[76:79], v[154:157], v[228:231], v[76:79]
	s_setprio 0
	s_setprio 1
	v_mfma_f32_16x16x32_bf16 v[112:115], v[158:161], v[182:185], v[112:115]
	v_mfma_f32_16x16x32_bf16 v[104:107], v[174:177], v[182:185], v[104:107]
	v_mfma_f32_16x16x32_bf16 v[96:99], v[158:161], v[202:205], v[96:99]
	v_mfma_f32_16x16x32_bf16 v[88:91], v[174:177], v[202:205], v[88:91]
	v_mfma_f32_16x16x32_bf16 v[80:83], v[158:161], v[210:213], v[80:83]
	v_mfma_f32_16x16x32_bf16 v[72:75], v[174:177], v[210:213], v[72:75]
	v_mfma_f32_16x16x32_bf16 v[68:71], v[158:161], v[224:227], v[68:71]
	v_mfma_f32_16x16x32_bf16 v[64:67], v[174:177], v[224:227], v[64:67]
	v_mfma_f32_16x16x32_bf16 v[112:115], v[162:165], v[198:201], v[112:115]
	v_mfma_f32_16x16x32_bf16 v[104:107], v[178:181], v[198:201], v[104:107]
	v_mfma_f32_16x16x32_bf16 v[96:99], v[162:165], v[206:209], v[96:99]
	v_mfma_f32_16x16x32_bf16 v[88:91], v[178:181], v[206:209], v[88:91]
	v_mfma_f32_16x16x32_bf16 v[80:83], v[162:165], v[214:217], v[80:83]
	v_mfma_f32_16x16x32_bf16 v[72:75], v[178:181], v[214:217], v[72:75]
	v_mfma_f32_16x16x32_bf16 v[68:71], v[162:165], v[228:231], v[68:71]
	v_mfma_f32_16x16x32_bf16 v[64:67], v[178:181], v[228:231], v[64:67]
	s_setprio 0
	s_barrier
	s_cmp_eq_u64 s[38:39], 0
	s_cselect_b32 s99, 4, -1
	s_cmp_eq_u32 s37, s99
	s_cselect_b32 s58, 0, s58
	s_mov_b32 m0, s13
	ds_read_b128 v[182:185], v141 offset:16384
	ds_read_b128 v[198:201], v141 offset:17408
	ds_read_b128 v[202:205], v141 offset:18432
	ds_read_b128 v[206:209], v141 offset:19456
	ds_read_b128 v[210:213], v141 offset:20480
	ds_read_b128 v[214:217], v141 offset:21504
	ds_read_b128 v[224:227], v141 offset:22528
	ds_read_b128 v[228:231], v141 offset:23552
	buffer_load_dwordx4 v129, s[56:59], s41 offen lds
	s_mov_b32 m0, s14
	s_add_i32 s43, s41, 0x20000
	buffer_load_dwordx4 v131, s[56:59], s41 offen lds
	s_mov_b32 m0, s15
	s_nop 0
	buffer_load_dwordx4 v129, s[56:59], s43 offen lds
	s_mov_b32 m0, s18
	s_nop 0
	buffer_load_dwordx4 v131, s[56:59], s43 offen lds
	s_mov_b32 m0, s12
	s_nop 0
	buffer_load_dwordx4 v128, s[56:59], s42 offen lds
	s_mov_b32 m0, s19
	s_nop 0
	buffer_load_dwordx4 v130, s[56:59], s42 offen lds
	s_waitcnt vmcnt(8)
	s_waitcnt lgkmcnt(0)
	s_barrier
	s_setprio 1
	s_waitcnt lgkmcnt(7)
	v_mfma_f32_16x16x32_bf16 v[60:63], v[142:145], v[182:185], v[60:63]
	v_mfma_f32_16x16x32_bf16 v[56:59], v[150:153], v[182:185], v[56:59]
	s_waitcnt lgkmcnt(5)
	v_mfma_f32_16x16x32_bf16 v[52:55], v[142:145], v[202:205], v[52:55]
	v_mfma_f32_16x16x32_bf16 v[44:47], v[150:153], v[202:205], v[44:47]
	s_waitcnt lgkmcnt(3)
	v_mfma_f32_16x16x32_bf16 v[36:39], v[142:145], v[210:213], v[36:39]
	v_mfma_f32_16x16x32_bf16 v[28:31], v[150:153], v[210:213], v[28:31]
	s_waitcnt lgkmcnt(1)
	v_mfma_f32_16x16x32_bf16 v[20:23], v[142:145], v[224:227], v[20:23]
	v_mfma_f32_16x16x32_bf16 v[12:15], v[150:153], v[224:227], v[12:15]
	v_mfma_f32_16x16x32_bf16 v[60:63], v[146:149], v[198:201], v[60:63]
	v_mfma_f32_16x16x32_bf16 v[56:59], v[154:157], v[198:201], v[56:59]
	v_mfma_f32_16x16x32_bf16 v[52:55], v[146:149], v[206:209], v[52:55]
	v_mfma_f32_16x16x32_bf16 v[44:47], v[154:157], v[206:209], v[44:47]
	v_mfma_f32_16x16x32_bf16 v[36:39], v[146:149], v[214:217], v[36:39]
	v_mfma_f32_16x16x32_bf16 v[28:31], v[154:157], v[214:217], v[28:31]
	s_waitcnt lgkmcnt(0)
	v_mfma_f32_16x16x32_bf16 v[20:23], v[146:149], v[228:231], v[20:23]
	v_mfma_f32_16x16x32_bf16 v[12:15], v[154:157], v[228:231], v[12:15]
	s_setprio 0
	s_setprio 1
	v_mfma_f32_16x16x32_bf16 v[48:51], v[158:161], v[182:185], v[48:51]
	v_mfma_f32_16x16x32_bf16 v[40:43], v[174:177], v[182:185], v[40:43]
	v_mfma_f32_16x16x32_bf16 v[32:35], v[158:161], v[202:205], v[32:35]
	v_mfma_f32_16x16x32_bf16 v[24:27], v[174:177], v[202:205], v[24:27]
	v_mfma_f32_16x16x32_bf16 v[16:19], v[158:161], v[210:213], v[16:19]
	v_mfma_f32_16x16x32_bf16 v[8:11], v[174:177], v[210:213], v[8:11]
	v_mfma_f32_16x16x32_bf16 v[4:7], v[158:161], v[224:227], v[4:7]
	v_mfma_f32_16x16x32_bf16 v[0:3], v[174:177], v[224:227], v[0:3]
	v_mfma_f32_16x16x32_bf16 v[48:51], v[162:165], v[198:201], v[48:51]
	v_mfma_f32_16x16x32_bf16 v[40:43], v[178:181], v[198:201], v[40:43]
	v_mfma_f32_16x16x32_bf16 v[32:35], v[162:165], v[206:209], v[32:35]
	v_mfma_f32_16x16x32_bf16 v[24:27], v[178:181], v[206:209], v[24:27]
	v_mfma_f32_16x16x32_bf16 v[16:19], v[162:165], v[214:217], v[16:19]
	v_mfma_f32_16x16x32_bf16 v[8:11], v[178:181], v[214:217], v[8:11]
	v_mfma_f32_16x16x32_bf16 v[4:7], v[162:165], v[228:231], v[4:7]
	v_mfma_f32_16x16x32_bf16 v[0:3], v[178:181], v[228:231], v[0:3]
	s_setprio 0
	s_barrier
	ds_read_b128 v[142:145], v140 offset:32768
	ds_read_b128 v[146:149], v140 offset:33792
	ds_read_b128 v[150:153], v140 offset:34816
	ds_read_b128 v[154:157], v140 offset:35840
	ds_read_b128 v[158:161], v140 offset:49152
	ds_read_b128 v[162:165], v140 offset:50176
	ds_read_b128 v[174:177], v140 offset:51200
	ds_read_b128 v[178:181], v140 offset:52224
	s_add_i32 s42, s42, 0x80000
	s_mov_b32 m0, s20
	ds_read_b128 v[182:185], v141 offset:32768
	ds_read_b128 v[198:201], v141 offset:33792
	ds_read_b128 v[202:205], v141 offset:34816
	ds_read_b128 v[206:209], v141 offset:35840
	ds_read_b128 v[210:213], v141 offset:36864
	ds_read_b128 v[214:217], v141 offset:37888
	ds_read_b128 v[224:227], v141 offset:38912
	ds_read_b128 v[228:231], v141 offset:39936
	buffer_load_dwordx4 v128, s[56:59], s42 offen lds
	s_mov_b32 m0, s21
	s_nop 0
	buffer_load_dwordx4 v130, s[56:59], s42 offen lds
	s_waitcnt vmcnt(8)
	s_waitcnt lgkmcnt(0)
	s_barrier
	s_setprio 1
	s_waitcnt lgkmcnt(7)
	v_mfma_f32_16x16x32_bf16 v[124:127], v[142:145], v[182:185], v[124:127]
	v_mfma_f32_16x16x32_bf16 v[120:123], v[150:153], v[182:185], v[120:123]
	s_waitcnt lgkmcnt(5)
	v_mfma_f32_16x16x32_bf16 v[116:119], v[142:145], v[202:205], v[116:119]
	v_mfma_f32_16x16x32_bf16 v[108:111], v[150:153], v[202:205], v[108:111]
	s_waitcnt lgkmcnt(3)
	v_mfma_f32_16x16x32_bf16 v[100:103], v[142:145], v[210:213], v[100:103]
	v_mfma_f32_16x16x32_bf16 v[92:95], v[150:153], v[210:213], v[92:95]
	s_waitcnt lgkmcnt(1)
	v_mfma_f32_16x16x32_bf16 v[84:87], v[142:145], v[224:227], v[84:87]
	v_mfma_f32_16x16x32_bf16 v[76:79], v[150:153], v[224:227], v[76:79]
	v_mfma_f32_16x16x32_bf16 v[124:127], v[146:149], v[198:201], v[124:127]
	v_mfma_f32_16x16x32_bf16 v[120:123], v[154:157], v[198:201], v[120:123]
	v_mfma_f32_16x16x32_bf16 v[116:119], v[146:149], v[206:209], v[116:119]
	v_mfma_f32_16x16x32_bf16 v[108:111], v[154:157], v[206:209], v[108:111]
	v_mfma_f32_16x16x32_bf16 v[100:103], v[146:149], v[214:217], v[100:103]
	v_mfma_f32_16x16x32_bf16 v[92:95], v[154:157], v[214:217], v[92:95]
	s_waitcnt lgkmcnt(0)
	v_mfma_f32_16x16x32_bf16 v[84:87], v[146:149], v[228:231], v[84:87]
	v_mfma_f32_16x16x32_bf16 v[76:79], v[154:157], v[228:231], v[76:79]
	s_setprio 0
	s_setprio 1
	v_mfma_f32_16x16x32_bf16 v[112:115], v[158:161], v[182:185], v[112:115]
	v_mfma_f32_16x16x32_bf16 v[104:107], v[174:177], v[182:185], v[104:107]
	v_mfma_f32_16x16x32_bf16 v[96:99], v[158:161], v[202:205], v[96:99]
	v_mfma_f32_16x16x32_bf16 v[88:91], v[174:177], v[202:205], v[88:91]
	v_mfma_f32_16x16x32_bf16 v[80:83], v[158:161], v[210:213], v[80:83]
	v_mfma_f32_16x16x32_bf16 v[72:75], v[174:177], v[210:213], v[72:75]
	v_mfma_f32_16x16x32_bf16 v[68:71], v[158:161], v[224:227], v[68:71]
	v_mfma_f32_16x16x32_bf16 v[64:67], v[174:177], v[224:227], v[64:67]
	v_mfma_f32_16x16x32_bf16 v[112:115], v[162:165], v[198:201], v[112:115]
	v_mfma_f32_16x16x32_bf16 v[104:107], v[178:181], v[198:201], v[104:107]
	v_mfma_f32_16x16x32_bf16 v[96:99], v[162:165], v[206:209], v[96:99]
	v_mfma_f32_16x16x32_bf16 v[88:91], v[178:181], v[206:209], v[88:91]
	v_mfma_f32_16x16x32_bf16 v[80:83], v[162:165], v[214:217], v[80:83]
	v_mfma_f32_16x16x32_bf16 v[72:75], v[178:181], v[214:217], v[72:75]
	v_mfma_f32_16x16x32_bf16 v[68:71], v[162:165], v[228:231], v[68:71]
	v_mfma_f32_16x16x32_bf16 v[64:67], v[178:181], v[228:231], v[64:67]
	s_setprio 0
	s_barrier
	s_mov_b32 m0, s22
	s_add_i32 s42, s41, 0x80
	ds_read_b128 v[182:185], v141 offset:49152
	ds_read_b128 v[198:201], v141 offset:50176
	ds_read_b128 v[202:205], v141 offset:51200
	ds_read_b128 v[206:209], v141 offset:52224
	ds_read_b128 v[210:213], v141 offset:53248
	ds_read_b128 v[214:217], v141 offset:54272
	ds_read_b128 v[224:227], v141 offset:55296
	ds_read_b128 v[228:231], v141 offset:56320
	buffer_load_dwordx4 v129, s[56:59], s42 offen lds
	s_mov_b32 m0, s23
	s_add_i32 s41, s41, 0x20080
	buffer_load_dwordx4 v131, s[56:59], s42 offen lds
	s_mov_b32 m0, s26
	s_nop 0
	buffer_load_dwordx4 v129, s[56:59], s41 offen lds
	s_mov_b32 m0, s27
	s_nop 0
	buffer_load_dwordx4 v131, s[56:59], s41 offen lds
	s_mov_b32 m0, s24
	s_nop 0
	buffer_load_dwordx4 v128, s[56:59], s40 offen lds
	s_mov_b32 m0, s25
	s_nop 0
	buffer_load_dwordx4 v130, s[56:59], s40 offen lds
	s_waitcnt vmcnt(8)
	s_waitcnt lgkmcnt(0)
	s_barrier
	s_setprio 1
	s_waitcnt lgkmcnt(7)
	v_mfma_f32_16x16x32_bf16 v[60:63], v[142:145], v[182:185], v[60:63]
	v_mfma_f32_16x16x32_bf16 v[56:59], v[150:153], v[182:185], v[56:59]
	s_waitcnt lgkmcnt(5)
	v_mfma_f32_16x16x32_bf16 v[52:55], v[142:145], v[202:205], v[52:55]
	v_mfma_f32_16x16x32_bf16 v[44:47], v[150:153], v[202:205], v[44:47]
	s_waitcnt lgkmcnt(3)
	v_mfma_f32_16x16x32_bf16 v[36:39], v[142:145], v[210:213], v[36:39]
	v_mfma_f32_16x16x32_bf16 v[28:31], v[150:153], v[210:213], v[28:31]
	s_waitcnt lgkmcnt(1)
	v_mfma_f32_16x16x32_bf16 v[20:23], v[142:145], v[224:227], v[20:23]
	v_mfma_f32_16x16x32_bf16 v[12:15], v[150:153], v[224:227], v[12:15]
	v_mfma_f32_16x16x32_bf16 v[60:63], v[146:149], v[198:201], v[60:63]
	v_mfma_f32_16x16x32_bf16 v[56:59], v[154:157], v[198:201], v[56:59]
	v_mfma_f32_16x16x32_bf16 v[52:55], v[146:149], v[206:209], v[52:55]
	v_mfma_f32_16x16x32_bf16 v[44:47], v[154:157], v[206:209], v[44:47]
	v_mfma_f32_16x16x32_bf16 v[36:39], v[146:149], v[214:217], v[36:39]
	v_mfma_f32_16x16x32_bf16 v[28:31], v[154:157], v[214:217], v[28:31]
	s_waitcnt lgkmcnt(0)
	v_mfma_f32_16x16x32_bf16 v[20:23], v[146:149], v[228:231], v[20:23]
	v_mfma_f32_16x16x32_bf16 v[12:15], v[154:157], v[228:231], v[12:15]
	s_setprio 0
	s_setprio 1
	v_mfma_f32_16x16x32_bf16 v[48:51], v[158:161], v[182:185], v[48:51]
	v_mfma_f32_16x16x32_bf16 v[40:43], v[174:177], v[182:185], v[40:43]
	v_mfma_f32_16x16x32_bf16 v[32:35], v[158:161], v[202:205], v[32:35]
	v_mfma_f32_16x16x32_bf16 v[24:27], v[174:177], v[202:205], v[24:27]
	v_mfma_f32_16x16x32_bf16 v[16:19], v[158:161], v[210:213], v[16:19]
	v_mfma_f32_16x16x32_bf16 v[8:11], v[174:177], v[210:213], v[8:11]
	v_mfma_f32_16x16x32_bf16 v[4:7], v[158:161], v[224:227], v[4:7]
	v_mfma_f32_16x16x32_bf16 v[0:3], v[174:177], v[224:227], v[0:3]
	v_mfma_f32_16x16x32_bf16 v[48:51], v[162:165], v[198:201], v[48:51]
	v_mfma_f32_16x16x32_bf16 v[40:43], v[178:181], v[198:201], v[40:43]
	v_mfma_f32_16x16x32_bf16 v[32:35], v[162:165], v[206:209], v[32:35]
	v_mfma_f32_16x16x32_bf16 v[24:27], v[178:181], v[206:209], v[24:27]
	v_mfma_f32_16x16x32_bf16 v[16:19], v[162:165], v[214:217], v[16:19]
	v_mfma_f32_16x16x32_bf16 v[8:11], v[178:181], v[214:217], v[8:11]
	v_mfma_f32_16x16x32_bf16 v[4:7], v[162:165], v[228:231], v[4:7]
	v_mfma_f32_16x16x32_bf16 v[0:3], v[178:181], v[228:231], v[0:3]
	s_setprio 0
	s_barrier
	s_add_i32 s37, s37, 2
	s_addk_i32 s10, 0x100
	s_addk_i32 s11, 0x100
	s_cmp_gt_u32 s37, 5
	s_cbranch_scc0 .LBB0_1238
	s_mov_b32 s58, s98
	s_and_b64 vcc, exec, s[2:3]
	s_cbranch_vccz .LBB0_1241
	s_barrier

.LBB0_1443:
	s_mov_b32 s98, s58
	ds_read_b128 v[16:19], v186
	ds_read_b128 v[20:23], v186 offset:1024
	ds_read_b128 v[24:27], v186 offset:2048
	ds_read_b128 v[28:31], v186 offset:3072
	ds_read_b128 v[0:3], v186 offset:16384
	ds_read_b128 v[4:7], v186 offset:17408
	ds_read_b128 v[8:11], v186 offset:18432
	ds_read_b128 v[12:15], v186 offset:19456
	s_add_i32 s72, s0, 0xfffc0080
	s_cmp_eq_u32 s81, 12
	s_cselect_b32 vcc_lo, s96, s72
	s_cselect_b32 s83, s97, s1
	s_add_i32 s82, vcc_lo, 0x80
	s_mov_b32 s56, s26
	s_mov_b32 m0, s87
	ds_read_b128 v[174:177], v198
	ds_read_b128 v[178:181], v198 offset:1024
	ds_read_b128 v[200:203], v198 offset:2048
	ds_read_b128 v[204:207], v198 offset:3072
	ds_read_b128 v[208:211], v198 offset:4096
	ds_read_b128 v[212:215], v198 offset:5120
	ds_read_b128 v[224:227], v198 offset:6144
	ds_read_b128 v[228:231], v198 offset:7168
	buffer_load_dwordx4 v160, s[56:59], s0 offen lds
	s_mov_b32 m0, s88
	s_nop 0
	buffer_load_dwordx4 v162, s[56:59], s0 offen lds
	s_waitcnt vmcnt(8)
	s_waitcnt lgkmcnt(0)
	s_barrier
	s_setprio 1
	s_waitcnt lgkmcnt(6)
	v_mfma_f32_16x16x128_f8f6f4 v[156:159], v[16:23], v[174:181], v[156:159]
	v_mfma_f32_16x16x128_f8f6f4 v[148:151], v[24:31], v[174:181], v[148:151]
	s_waitcnt lgkmcnt(4)
	v_mfma_f32_16x16x128_f8f6f4 v[140:143], v[16:23], v[200:207], v[140:143]
	v_mfma_f32_16x16x128_f8f6f4 v[132:135], v[24:31], v[200:207], v[132:135]
	s_waitcnt lgkmcnt(2)
	v_mfma_f32_16x16x128_f8f6f4 v[124:127], v[16:23], v[208:215], v[124:127]
	v_mfma_f32_16x16x128_f8f6f4 v[116:119], v[24:31], v[208:215], v[116:119]
	s_waitcnt lgkmcnt(0)
	v_mfma_f32_16x16x128_f8f6f4 v[108:111], v[16:23], v[224:231], v[108:111]
	v_mfma_f32_16x16x128_f8f6f4 v[100:103], v[24:31], v[224:231], v[100:103]
	s_setprio 0
	s_setprio 1
	v_mfma_f32_16x16x128_f8f6f4 v[152:155], v[0:7], v[174:181], v[152:155]
	v_mfma_f32_16x16x128_f8f6f4 v[144:147], v[8:15], v[174:181], v[144:147]
	v_mfma_f32_16x16x128_f8f6f4 v[136:139], v[0:7], v[200:207], v[136:139]
	v_mfma_f32_16x16x128_f8f6f4 v[128:131], v[8:15], v[200:207], v[128:131]
	v_mfma_f32_16x16x128_f8f6f4 v[120:123], v[0:7], v[208:215], v[120:123]
	v_mfma_f32_16x16x128_f8f6f4 v[112:115], v[8:15], v[208:215], v[112:115]
	v_mfma_f32_16x16x128_f8f6f4 v[104:107], v[0:7], v[224:231], v[104:107]
	v_mfma_f32_16x16x128_f8f6f4 v[96:99], v[8:15], v[224:231], v[96:99]
	s_setprio 0
	s_barrier
	s_cmp_eq_u64 s[36:37], 0
	s_cselect_b32 s99, 12, -1
	s_cmp_eq_u32 s81, s99
	s_cselect_b32 s58, 0, s58
	s_mov_b32 m0, s46
	ds_read_b128 v[174:177], v198 offset:16384
	ds_read_b128 v[178:181], v198 offset:17408
	ds_read_b128 v[200:203], v198 offset:18432
	ds_read_b128 v[204:207], v198 offset:19456
	ds_read_b128 v[208:211], v198 offset:20480
	ds_read_b128 v[212:215], v198 offset:21504
	ds_read_b128 v[224:227], v198 offset:22528
	ds_read_b128 v[228:231], v198 offset:23552
	buffer_load_dwordx4 v161, s[56:59], s83 offen lds
	s_mov_b32 m0, s47
	s_add_i32 vcc_hi, s83, 0x40000
	buffer_load_dwordx4 v163, s[56:59], s83 offen lds
	s_mov_b32 m0, s48
	s_nop 0
	buffer_load_dwordx4 v161, s[56:59], vcc_hi offen lds
	s_mov_b32 m0, s49
	s_nop 0
	buffer_load_dwordx4 v163, s[56:59], vcc_hi offen lds
	s_mov_b32 m0, s45
	s_nop 0
	buffer_load_dwordx4 v160, s[56:59], vcc_lo offen lds
	s_mov_b32 m0, s50
	s_nop 0
	buffer_load_dwordx4 v162, s[56:59], vcc_lo offen lds
	s_waitcnt vmcnt(8)
	s_waitcnt lgkmcnt(0)
	s_barrier
	s_setprio 1
	s_waitcnt lgkmcnt(6)
	v_mfma_f32_16x16x128_f8f6f4 v[92:95], v[16:23], v[174:181], v[92:95]
	v_mfma_f32_16x16x128_f8f6f4 v[84:87], v[24:31], v[174:181], v[84:87]
	s_waitcnt lgkmcnt(4)
	v_mfma_f32_16x16x128_f8f6f4 v[76:79], v[16:23], v[200:207], v[76:79]
	v_mfma_f32_16x16x128_f8f6f4 v[68:71], v[24:31], v[200:207], v[68:71]
	s_waitcnt lgkmcnt(2)
	v_mfma_f32_16x16x128_f8f6f4 v[60:63], v[16:23], v[208:215], v[60:63]
	v_mfma_f32_16x16x128_f8f6f4 v[52:55], v[24:31], v[208:215], v[52:55]
	s_waitcnt lgkmcnt(0)
	v_mfma_f32_16x16x128_f8f6f4 v[44:47], v[16:23], v[224:231], v[44:47]
	v_mfma_f32_16x16x128_f8f6f4 v[36:39], v[24:31], v[224:231], v[36:39]
	s_setprio 0
	s_setprio 1
	v_mfma_f32_16x16x128_f8f6f4 v[88:91], v[0:7], v[174:181], v[88:91]
	v_mfma_f32_16x16x128_f8f6f4 v[80:83], v[8:15], v[174:181], v[80:83]
	v_mfma_f32_16x16x128_f8f6f4 v[72:75], v[0:7], v[200:207], v[72:75]
	v_mfma_f32_16x16x128_f8f6f4 v[64:67], v[8:15], v[200:207], v[64:67]
	v_mfma_f32_16x16x128_f8f6f4 v[56:59], v[0:7], v[208:215], v[56:59]
	v_mfma_f32_16x16x128_f8f6f4 v[48:51], v[8:15], v[208:215], v[48:51]
	v_mfma_f32_16x16x128_f8f6f4 v[40:43], v[0:7], v[224:231], v[40:43]
	v_mfma_f32_16x16x128_f8f6f4 v[32:35], v[8:15], v[224:231], v[32:35]
	s_setprio 0
	s_barrier
	ds_read_b128 v[0:3], v186 offset:32768
	ds_read_b128 v[4:7], v186 offset:33792
	ds_read_b128 v[8:11], v186 offset:34816
	ds_read_b128 v[12:15], v186 offset:35840
	ds_read_b128 v[16:19], v186 offset:49152
	ds_read_b128 v[20:23], v186 offset:50176
	ds_read_b128 v[24:27], v186 offset:51200
	ds_read_b128 v[28:31], v186 offset:52224
	s_add_i32 vcc_lo, vcc_lo, 0x40000
	s_mov_b32 m0, s51
	ds_read_b128 v[174:177], v198 offset:32768
	ds_read_b128 v[178:181], v198 offset:33792
	ds_read_b128 v[200:203], v198 offset:34816
	ds_read_b128 v[204:207], v198 offset:35840
	ds_read_b128 v[208:211], v198 offset:36864
	ds_read_b128 v[212:215], v198 offset:37888
	ds_read_b128 v[224:227], v198 offset:38912
	ds_read_b128 v[228:231], v198 offset:39936
	buffer_load_dwordx4 v160, s[56:59], vcc_lo offen lds
	s_mov_b32 m0, s52
	s_nop 0
	buffer_load_dwordx4 v162, s[56:59], vcc_lo offen lds
	s_waitcnt vmcnt(8)
	s_waitcnt lgkmcnt(0)
	s_barrier
	s_setprio 1
	s_waitcnt lgkmcnt(6)
	v_mfma_f32_16x16x128_f8f6f4 v[156:159], v[0:7], v[174:181], v[156:159]
	v_mfma_f32_16x16x128_f8f6f4 v[148:151], v[8:15], v[174:181], v[148:151]
	s_waitcnt lgkmcnt(4)
	v_mfma_f32_16x16x128_f8f6f4 v[140:143], v[0:7], v[200:207], v[140:143]
	v_mfma_f32_16x16x128_f8f6f4 v[132:135], v[8:15], v[200:207], v[132:135]
	s_waitcnt lgkmcnt(2)
	v_mfma_f32_16x16x128_f8f6f4 v[124:127], v[0:7], v[208:215], v[124:127]
	v_mfma_f32_16x16x128_f8f6f4 v[116:119], v[8:15], v[208:215], v[116:119]
	s_waitcnt lgkmcnt(0)
	v_mfma_f32_16x16x128_f8f6f4 v[108:111], v[0:7], v[224:231], v[108:111]
	v_mfma_f32_16x16x128_f8f6f4 v[100:103], v[8:15], v[224:231], v[100:103]
	s_setprio 0
	s_setprio 1
	v_mfma_f32_16x16x128_f8f6f4 v[152:155], v[16:23], v[174:181], v[152:155]
	v_mfma_f32_16x16x128_f8f6f4 v[144:147], v[24:31], v[174:181], v[144:147]
	v_mfma_f32_16x16x128_f8f6f4 v[136:139], v[16:23], v[200:207], v[136:139]
	v_mfma_f32_16x16x128_f8f6f4 v[128:131], v[24:31], v[200:207], v[128:131]
	v_mfma_f32_16x16x128_f8f6f4 v[120:123], v[16:23], v[208:215], v[120:123]
	v_mfma_f32_16x16x128_f8f6f4 v[112:115], v[24:31], v[208:215], v[112:115]
	v_mfma_f32_16x16x128_f8f6f4 v[104:107], v[16:23], v[224:231], v[104:107]
	v_mfma_f32_16x16x128_f8f6f4 v[96:99], v[24:31], v[224:231], v[96:99]
	s_setprio 0
	s_barrier
	s_mov_b32 m0, s76
	s_add_i32 vcc_lo, s83, 0x80
	ds_read_b128 v[174:177], v198 offset:49152
	ds_read_b128 v[178:181], v198 offset:50176
	ds_read_b128 v[200:203], v198 offset:51200
	ds_read_b128 v[204:207], v198 offset:52224
	ds_read_b128 v[208:211], v198 offset:53248
	ds_read_b128 v[212:215], v198 offset:54272
	ds_read_b128 v[224:227], v198 offset:55296
	ds_read_b128 v[228:231], v198 offset:56320
	buffer_load_dwordx4 v161, s[56:59], vcc_lo offen lds
	s_mov_b32 m0, s77
	s_add_i32 s83, s83, 0x40080
	buffer_load_dwordx4 v163, s[56:59], vcc_lo offen lds
	s_mov_b32 m0, s85
	s_nop 0
	buffer_load_dwordx4 v161, s[56:59], s83 offen lds
	s_mov_b32 m0, s86
	s_nop 0
	buffer_load_dwordx4 v163, s[56:59], s83 offen lds
	s_mov_b32 m0, s78
	s_nop 0
	buffer_load_dwordx4 v160, s[56:59], s82 offen lds
	s_mov_b32 m0, s79
	s_nop 0
	buffer_load_dwordx4 v162, s[56:59], s82 offen lds
	s_waitcnt vmcnt(8)
	s_waitcnt lgkmcnt(0)
	s_barrier
	s_setprio 1
	s_waitcnt lgkmcnt(6)
	v_mfma_f32_16x16x128_f8f6f4 v[92:95], v[0:7], v[174:181], v[92:95]
	v_mfma_f32_16x16x128_f8f6f4 v[84:87], v[8:15], v[174:181], v[84:87]
	s_waitcnt lgkmcnt(4)
	v_mfma_f32_16x16x128_f8f6f4 v[76:79], v[0:7], v[200:207], v[76:79]
	v_mfma_f32_16x16x128_f8f6f4 v[68:71], v[8:15], v[200:207], v[68:71]
	s_waitcnt lgkmcnt(2)
	v_mfma_f32_16x16x128_f8f6f4 v[60:63], v[0:7], v[208:215], v[60:63]
	v_mfma_f32_16x16x128_f8f6f4 v[52:55], v[8:15], v[208:215], v[52:55]
	s_waitcnt lgkmcnt(0)
	v_mfma_f32_16x16x128_f8f6f4 v[44:47], v[0:7], v[224:231], v[44:47]
	v_mfma_f32_16x16x128_f8f6f4 v[36:39], v[8:15], v[224:231], v[36:39]
	s_setprio 0
	s_setprio 1
	v_mfma_f32_16x16x128_f8f6f4 v[88:91], v[16:23], v[174:181], v[88:91]
	v_mfma_f32_16x16x128_f8f6f4 v[80:83], v[24:31], v[174:181], v[80:83]
	v_mfma_f32_16x16x128_f8f6f4 v[72:75], v[16:23], v[200:207], v[72:75]
	v_mfma_f32_16x16x128_f8f6f4 v[64:67], v[24:31], v[200:207], v[64:67]
	v_mfma_f32_16x16x128_f8f6f4 v[56:59], v[16:23], v[208:215], v[56:59]
	v_mfma_f32_16x16x128_f8f6f4 v[48:51], v[24:31], v[208:215], v[48:51]
	v_mfma_f32_16x16x128_f8f6f4 v[40:43], v[16:23], v[224:231], v[40:43]
	v_mfma_f32_16x16x128_f8f6f4 v[32:35], v[24:31], v[224:231], v[32:35]
	s_setprio 0
	s_barrier
	s_add_i32 s81, s81, 2
	s_addk_i32 s0, 0x100
	s_addk_i32 s1, 0x100
	s_cmp_gt_u32 s81, 13
	s_cbranch_scc0 .LBB0_1443
	s_mov_b32 s58, s98
	s_and_b64 vcc, exec, s[70:71]
	s_cbranch_vccz .LBB0_1446
	s_barrier

.LBB0_1667:
	s_mov_b32 s98, s58
	ds_read_b128 v[16:19], v198
	ds_read_b128 v[20:23], v198 offset:1024
	ds_read_b128 v[24:27], v198 offset:2048
	ds_read_b128 v[28:31], v198 offset:3072
	ds_read_b128 v[0:3], v198 offset:16384
	ds_read_b128 v[4:7], v198 offset:17408
	ds_read_b128 v[8:11], v198 offset:18432
	ds_read_b128 v[12:15], v198 offset:19456
	s_add_i32 s55, s0, 0xfffd0080
	s_cmp_eq_u32 s33, 8
	s_cselect_b32 s81, s40, s55
	s_cselect_b32 s80, s41, s1
	s_add_i32 s55, s81, 0x80
	s_mov_b32 s56, s78
	s_mov_b32 m0, s20
	ds_read_b128 v[174:177], v199
	ds_read_b128 v[178:181], v199 offset:1024
	ds_read_b128 v[200:203], v199 offset:2048
	ds_read_b128 v[204:207], v199 offset:3072
	ds_read_b128 v[208:211], v199 offset:4096
	ds_read_b128 v[212:215], v199 offset:5120
	ds_read_b128 v[224:227], v199 offset:6144
	ds_read_b128 v[228:231], v199 offset:7168
	buffer_load_dwordx4 v162, s[56:59], s0 offen lds
	s_mov_b32 m0, s19
	s_nop 0
	buffer_load_dwordx4 v164, s[56:59], s0 offen lds
	s_waitcnt vmcnt(8)
	s_waitcnt lgkmcnt(0)
	s_barrier
	s_setprio 1
	s_waitcnt lgkmcnt(6)
	v_mfma_f32_16x16x128_f8f6f4 v[156:159], v[16:23], v[174:181], v[156:159]
	v_mfma_f32_16x16x128_f8f6f4 v[152:155], v[24:31], v[174:181], v[152:155]
	s_waitcnt lgkmcnt(4)
	v_mfma_f32_16x16x128_f8f6f4 v[140:143], v[16:23], v[200:207], v[140:143]
	v_mfma_f32_16x16x128_f8f6f4 v[136:139], v[24:31], v[200:207], v[136:139]
	s_waitcnt lgkmcnt(2)
	v_mfma_f32_16x16x128_f8f6f4 v[124:127], v[16:23], v[208:215], v[124:127]
	v_mfma_f32_16x16x128_f8f6f4 v[120:123], v[24:31], v[208:215], v[120:123]
	s_waitcnt lgkmcnt(0)
	v_mfma_f32_16x16x128_f8f6f4 v[108:111], v[16:23], v[224:231], v[108:111]
	v_mfma_f32_16x16x128_f8f6f4 v[104:107], v[24:31], v[224:231], v[104:107]
	s_setprio 0
	s_setprio 1
	v_mfma_f32_16x16x128_f8f6f4 v[148:151], v[0:7], v[174:181], v[148:151]
	v_mfma_f32_16x16x128_f8f6f4 v[144:147], v[8:15], v[174:181], v[144:147]
	v_mfma_f32_16x16x128_f8f6f4 v[132:135], v[0:7], v[200:207], v[132:135]
	v_mfma_f32_16x16x128_f8f6f4 v[128:131], v[8:15], v[200:207], v[128:131]
	v_mfma_f32_16x16x128_f8f6f4 v[116:119], v[0:7], v[208:215], v[116:119]
	v_mfma_f32_16x16x128_f8f6f4 v[112:115], v[8:15], v[208:215], v[112:115]
	v_mfma_f32_16x16x128_f8f6f4 v[100:103], v[0:7], v[224:231], v[100:103]
	v_mfma_f32_16x16x128_f8f6f4 v[96:99], v[8:15], v[224:231], v[96:99]
	s_setprio 0
	s_barrier
	s_cmp_eq_u64 s[36:37], 0
	s_cselect_b32 s99, 8, -1
	s_cmp_eq_u32 s33, s99
	s_cselect_b32 s58, 0, s58
	s_mov_b32 m0, s85
	ds_read_b128 v[174:177], v199 offset:16384
	ds_read_b128 v[178:181], v199 offset:17408
	ds_read_b128 v[200:203], v199 offset:18432
	ds_read_b128 v[204:207], v199 offset:19456
	ds_read_b128 v[208:211], v199 offset:20480
	ds_read_b128 v[212:215], v199 offset:21504
	ds_read_b128 v[224:227], v199 offset:22528
	ds_read_b128 v[228:231], v199 offset:23552
	buffer_load_dwordx4 v161, s[56:59], s80 offen lds
	s_mov_b32 m0, s86
	s_add_i32 s82, s80, 0x30000
	buffer_load_dwordx4 v163, s[56:59], s80 offen lds
	s_mov_b32 m0, s87
	s_nop 0
	buffer_load_dwordx4 v161, s[56:59], s82 offen lds
	s_mov_b32 m0, s88
	s_nop 0
	buffer_load_dwordx4 v163, s[56:59], s82 offen lds
	s_mov_b32 m0, s18
	s_nop 0
	buffer_load_dwordx4 v162, s[56:59], s81 offen lds
	s_mov_b32 m0, s89
	s_nop 0
	buffer_load_dwordx4 v164, s[56:59], s81 offen lds
	s_waitcnt vmcnt(8)
	s_waitcnt lgkmcnt(0)
	s_barrier
	s_setprio 1
	s_waitcnt lgkmcnt(6)
	v_mfma_f32_16x16x128_f8f6f4 v[92:95], v[16:23], v[174:181], v[92:95]
	v_mfma_f32_16x16x128_f8f6f4 v[88:91], v[24:31], v[174:181], v[88:91]
	s_waitcnt lgkmcnt(4)
	v_mfma_f32_16x16x128_f8f6f4 v[76:79], v[16:23], v[200:207], v[76:79]
	v_mfma_f32_16x16x128_f8f6f4 v[72:75], v[24:31], v[200:207], v[72:75]
	s_waitcnt lgkmcnt(2)
	v_mfma_f32_16x16x128_f8f6f4 v[60:63], v[16:23], v[208:215], v[60:63]
	v_mfma_f32_16x16x128_f8f6f4 v[56:59], v[24:31], v[208:215], v[56:59]
	s_waitcnt lgkmcnt(0)
	v_mfma_f32_16x16x128_f8f6f4 v[44:47], v[16:23], v[224:231], v[44:47]
	v_mfma_f32_16x16x128_f8f6f4 v[40:43], v[24:31], v[224:231], v[40:43]
	s_setprio 0
	s_setprio 1
	v_mfma_f32_16x16x128_f8f6f4 v[84:87], v[0:7], v[174:181], v[84:87]
	v_mfma_f32_16x16x128_f8f6f4 v[80:83], v[8:15], v[174:181], v[80:83]
	v_mfma_f32_16x16x128_f8f6f4 v[68:71], v[0:7], v[200:207], v[68:71]
	v_mfma_f32_16x16x128_f8f6f4 v[64:67], v[8:15], v[200:207], v[64:67]
	v_mfma_f32_16x16x128_f8f6f4 v[52:55], v[0:7], v[208:215], v[52:55]
	v_mfma_f32_16x16x128_f8f6f4 v[48:51], v[8:15], v[208:215], v[48:51]
	v_mfma_f32_16x16x128_f8f6f4 v[36:39], v[0:7], v[224:231], v[36:39]
	v_mfma_f32_16x16x128_f8f6f4 v[32:35], v[8:15], v[224:231], v[32:35]
	s_setprio 0
	s_barrier
	ds_read_b128 v[0:3], v198 offset:32768
	ds_read_b128 v[4:7], v198 offset:33792
	ds_read_b128 v[8:11], v198 offset:34816
	ds_read_b128 v[12:15], v198 offset:35840
	ds_read_b128 v[16:19], v198 offset:49152
	ds_read_b128 v[20:23], v198 offset:50176
	ds_read_b128 v[24:27], v198 offset:51200
	ds_read_b128 v[28:31], v198 offset:52224
	s_add_i32 s81, s81, 0x30000
	s_mov_b32 m0, s91
	ds_read_b128 v[174:177], v199 offset:32768
	ds_read_b128 v[178:181], v199 offset:33792
	ds_read_b128 v[200:203], v199 offset:34816
	ds_read_b128 v[204:207], v199 offset:35840
	ds_read_b128 v[208:211], v199 offset:36864
	ds_read_b128 v[212:215], v199 offset:37888
	ds_read_b128 v[224:227], v199 offset:38912
	ds_read_b128 v[228:231], v199 offset:39936
	buffer_load_dwordx4 v162, s[56:59], s81 offen lds
	s_mov_b32 m0, s92
	s_nop 0
	buffer_load_dwordx4 v164, s[56:59], s81 offen lds
	s_waitcnt vmcnt(8)
	s_waitcnt lgkmcnt(0)
	s_barrier
	s_setprio 1
	s_waitcnt lgkmcnt(6)
	v_mfma_f32_16x16x128_f8f6f4 v[156:159], v[0:7], v[174:181], v[156:159]
	v_mfma_f32_16x16x128_f8f6f4 v[152:155], v[8:15], v[174:181], v[152:155]
	s_waitcnt lgkmcnt(4)
	v_mfma_f32_16x16x128_f8f6f4 v[140:143], v[0:7], v[200:207], v[140:143]
	v_mfma_f32_16x16x128_f8f6f4 v[136:139], v[8:15], v[200:207], v[136:139]
	s_waitcnt lgkmcnt(2)
	v_mfma_f32_16x16x128_f8f6f4 v[124:127], v[0:7], v[208:215], v[124:127]
	v_mfma_f32_16x16x128_f8f6f4 v[120:123], v[8:15], v[208:215], v[120:123]
	s_waitcnt lgkmcnt(0)
	v_mfma_f32_16x16x128_f8f6f4 v[108:111], v[0:7], v[224:231], v[108:111]
	v_mfma_f32_16x16x128_f8f6f4 v[104:107], v[8:15], v[224:231], v[104:107]
	s_setprio 0
	s_setprio 1
	v_mfma_f32_16x16x128_f8f6f4 v[148:151], v[16:23], v[174:181], v[148:151]
	v_mfma_f32_16x16x128_f8f6f4 v[144:147], v[24:31], v[174:181], v[144:147]
	v_mfma_f32_16x16x128_f8f6f4 v[132:135], v[16:23], v[200:207], v[132:135]
	v_mfma_f32_16x16x128_f8f6f4 v[128:131], v[24:31], v[200:207], v[128:131]
	v_mfma_f32_16x16x128_f8f6f4 v[116:119], v[16:23], v[208:215], v[116:119]
	v_mfma_f32_16x16x128_f8f6f4 v[112:115], v[24:31], v[208:215], v[112:115]
	v_mfma_f32_16x16x128_f8f6f4 v[100:103], v[16:23], v[224:231], v[100:103]
	v_mfma_f32_16x16x128_f8f6f4 v[96:99], v[24:31], v[224:231], v[96:99]
	s_setprio 0
	s_barrier
	s_mov_b32 m0, s93
	s_add_i32 s81, s80, 0x80
	ds_read_b128 v[174:177], v199 offset:49152
	ds_read_b128 v[178:181], v199 offset:50176
	ds_read_b128 v[200:203], v199 offset:51200
	ds_read_b128 v[204:207], v199 offset:52224
	ds_read_b128 v[208:211], v199 offset:53248
	ds_read_b128 v[212:215], v199 offset:54272
	ds_read_b128 v[224:227], v199 offset:55296
	ds_read_b128 v[228:231], v199 offset:56320
	buffer_load_dwordx4 v161, s[56:59], s81 offen lds
	s_mov_b32 m0, s95
	s_add_i32 s80, s80, 0x30080
	buffer_load_dwordx4 v163, s[56:59], s81 offen lds
	s_mov_b32 m0, s83
	s_nop 0
	buffer_load_dwordx4 v161, s[56:59], s80 offen lds
	s_mov_b32 m0, s21
	s_nop 0
	buffer_load_dwordx4 v163, s[56:59], s80 offen lds
	s_mov_b32 m0, s96
	s_nop 0
	buffer_load_dwordx4 v162, s[56:59], s55 offen lds
	s_mov_b32 m0, s97
	s_nop 0
	buffer_load_dwordx4 v164, s[56:59], s55 offen lds
	s_waitcnt vmcnt(8)
	s_waitcnt lgkmcnt(0)
	s_barrier
	s_setprio 1
	s_waitcnt lgkmcnt(6)
	v_mfma_f32_16x16x128_f8f6f4 v[92:95], v[0:7], v[174:181], v[92:95]
	v_mfma_f32_16x16x128_f8f6f4 v[88:91], v[8:15], v[174:181], v[88:91]
	s_waitcnt lgkmcnt(4)
	v_mfma_f32_16x16x128_f8f6f4 v[76:79], v[0:7], v[200:207], v[76:79]
	v_mfma_f32_16x16x128_f8f6f4 v[72:75], v[8:15], v[200:207], v[72:75]
	s_waitcnt lgkmcnt(2)
	v_mfma_f32_16x16x128_f8f6f4 v[60:63], v[0:7], v[208:215], v[60:63]
	v_mfma_f32_16x16x128_f8f6f4 v[56:59], v[8:15], v[208:215], v[56:59]
	s_waitcnt lgkmcnt(0)
	v_mfma_f32_16x16x128_f8f6f4 v[44:47], v[0:7], v[224:231], v[44:47]
	v_mfma_f32_16x16x128_f8f6f4 v[40:43], v[8:15], v[224:231], v[40:43]
	s_setprio 0
	s_setprio 1
	v_mfma_f32_16x16x128_f8f6f4 v[84:87], v[16:23], v[174:181], v[84:87]
	v_mfma_f32_16x16x128_f8f6f4 v[80:83], v[24:31], v[174:181], v[80:83]
	v_mfma_f32_16x16x128_f8f6f4 v[68:71], v[16:23], v[200:207], v[68:71]
	v_mfma_f32_16x16x128_f8f6f4 v[64:67], v[24:31], v[200:207], v[64:67]
	v_mfma_f32_16x16x128_f8f6f4 v[52:55], v[16:23], v[208:215], v[52:55]
	v_mfma_f32_16x16x128_f8f6f4 v[48:51], v[24:31], v[208:215], v[48:51]
	v_mfma_f32_16x16x128_f8f6f4 v[36:39], v[16:23], v[224:231], v[36:39]
	v_mfma_f32_16x16x128_f8f6f4 v[32:35], v[24:31], v[224:231], v[32:35]
	s_setprio 0
	s_barrier
	s_add_i32 s33, s33, 2
	s_addk_i32 s0, 0x100
	s_addk_i32 s1, 0x100
	s_cmp_gt_u32 s33, 9
	s_cbranch_scc0 .LBB0_1667
	s_mov_b32 s58, s98
	v_readlane_b32 s64, v253, 40
	s_and_b64 vcc, exec, s[24:25]
	v_readlane_b32 s65, v253, 41
	s_cbranch_vccz .LBB0_1670
	s_barrier
